# gathers: the mid-step u-row load block moved out of the priority-raised butterfly+gelu chain to the start of the bulk decode part (waits recounted, simulation-checked)
# speedup vs baseline: 1.0009x; 1.0009x over previous
.LBB0_763:
	s_cmpk_ge_i32 s58, 0x70
	s_cselect_b64 s[12:13], -1, 0
	ds_bpermute_b32 v84, v93, v92
	s_and_b64 vcc, s[12:13], s[48:49]
	v_cndmask_b32_e32 v104, v0, v94, vcc
	v_ashrrev_i32_e32 v105, 31, v104
	s_add_i32 s12, s58, 16
	s_and_b32 s12, s12, 0x70
	v_lshlrev_b64 v[104:105], 9, v[104:105]
	v_lshl_add_u64 v[104:105], s[94:95], 0, v[104:105]
	s_lshl_b32 s36, s12, 2
	s_waitcnt lgkmcnt(0)
	s_waitcnt vmcnt(32)
	v_mov_b32_e32 v92, v122
	v_ashrrev_i32_e32 v85, 31, v84
	v_lshl_add_u64 v[104:105], v[104:105], 0, s[36:37]
	v_lshl_add_u64 v[84:85], v[84:85], 3, s[8:9]
	v_lshl_add_u64 v[104:105], v[104:105], 0, v[144:145]
	global_load_dwordx2 v[84:85], v[84:85], off
	s_nop 0
	global_load_dword v86, v[72:73], off
	global_load_dword v122, v[104:105], off
	s_waitcnt vmcnt(19)
	v_dot8_i32_i4 v87, v8, v1, 0
	v_dot8_i32_i4 v104, v8, v88, 0
	v_dot8_i32_i4 v87, v9, v89, v87
	v_dot8_i32_i4 v104, v9, v90, v104
	s_waitcnt vmcnt(19)
	v_dot8_i32_i4 v9, v10, v88, 0
	v_dot8_i32_i4 v9, v11, v90, v9
	v_lshl_add_u32 v87, v87, 4, v104
	v_dot8_i32_i4 v8, v10, v1, 0
	v_dot8_i32_i4 v8, v11, v89, v8
	s_add_i32 s58, s58, 16
	v_lshl_add_u64 v[72:73], v[72:73], 0, 64
	s_nop 0
	v_lshl_add_u32 v104, v8, 4, v9
	v_dot8_i32_i4 v8, v12, v1, 0
	v_dot8_i32_i4 v9, v12, v88, 0
	v_dot8_i32_i4 v8, v13, v89, v8
	v_dot8_i32_i4 v9, v13, v90, v9
	v_readlane_b32 s12, v92, 0
	v_readlane_b32 s28, v92, 8
	v_readlane_b32 s30, v92, 9
	v_lshl_add_u32 v105, v8, 4, v9
	v_dot8_i32_i4 v8, v14, v1, 0
	v_dot8_i32_i4 v9, v14, v88, 0
	v_dot8_i32_i4 v8, v15, v89, v8
	v_dot8_i32_i4 v9, v15, v90, v9
	s_ashr_i32 s13, s12, 31
	v_readlane_b32 s14, v92, 1
	s_ashr_i32 s29, s28, 31
	v_lshl_add_u32 v106, v8, 4, v9
	v_dot8_i32_i4 v8, v16, v1, 0
	v_dot8_i32_i4 v9, v16, v88, 0
	v_dot8_i32_i4 v8, v17, v89, v8
	v_dot8_i32_i4 v9, v17, v90, v9
	s_ashr_i32 s31, s30, 31
	v_readlane_b32 s34, v92, 10
	s_lshl_b64 s[12:13], s[12:13], 9
	v_lshl_add_u32 v107, v8, 4, v9
	v_dot8_i32_i4 v8, v18, v1, 0
	v_dot8_i32_i4 v9, v18, v88, 0
	v_dot8_i32_i4 v8, v19, v89, v8
	v_dot8_i32_i4 v9, v19, v90, v9
	s_ashr_i32 s15, s14, 31
	v_readlane_b32 s16, v92, 2
	s_lshl_b64 s[28:29], s[28:29], 9
	v_lshl_add_u32 v108, v8, 4, v9
	v_dot8_i32_i4 v8, v20, v1, 0
	v_dot8_i32_i4 v9, v20, v88, 0
	v_dot8_i32_i4 v8, v21, v89, v8
	v_dot8_i32_i4 v9, v21, v90, v9
	s_lshl_b64 s[30:31], s[30:31], 9
	s_ashr_i32 s35, s34, 31
	v_readlane_b32 s38, v92, 11
	v_lshl_add_u32 v109, v8, 4, v9
	v_dot8_i32_i4 v8, v22, v1, 0
	v_dot8_i32_i4 v9, v22, v88, 0
	v_dot8_i32_i4 v8, v23, v89, v8
	v_dot8_i32_i4 v9, v23, v90, v9
	s_lshl_b64 s[14:15], s[14:15], 9
	s_ashr_i32 s17, s16, 31
	v_readlane_b32 s18, v92, 3
	v_lshl_add_u32 v110, v8, 4, v9
	v_dot8_i32_i4 v8, v24, v1, 0
	v_dot8_i32_i4 v9, v24, v88, 0
	v_dot8_i32_i4 v8, v25, v89, v8
	v_dot8_i32_i4 v9, v25, v90, v9
	s_lshl_b64 s[34:35], s[34:35], 9
	s_ashr_i32 s39, s38, 31
	s_nop 0
	v_lshl_add_u32 v111, v8, 4, v9
	v_dot8_i32_i4 v8, v38, v1, 0
	v_dot8_i32_i4 v9, v38, v88, 0
	v_dot8_i32_i4 v8, v39, v89, v8
	v_dot8_i32_i4 v9, v39, v90, v9
	s_setprio 2
	v_permlane32_swap_b32 v87, v111
	s_nop 1
	v_lshl_add_u32 v112, v8, 4, v9
	v_dot8_i32_i4 v8, v50, v1, 0
	v_dot8_i32_i4 v9, v50, v88, 0
	v_dot8_i32_i4 v8, v51, v89, v8
	v_dot8_i32_i4 v9, v51, v90, v9
	s_waitcnt lgkmcnt(0)
	v_add_u32_e32 v87, v87, v111
	v_permlane32_swap_b32 v104, v112
	v_lshl_add_u32 v113, v8, 4, v9
	v_dot8_i32_i4 v8, v48, v1, 0
	v_dot8_i32_i4 v9, v48, v88, 0
	v_dot8_i32_i4 v8, v49, v89, v8
	v_dot8_i32_i4 v9, v49, v90, v9
	s_waitcnt lgkmcnt(0)
	v_add_u32_e32 v104, v104, v112
	v_permlane32_swap_b32 v105, v113
	v_lshl_add_u32 v114, v8, 4, v9
	v_dot8_i32_i4 v8, v46, v1, 0
	v_dot8_i32_i4 v9, v46, v88, 0
	v_dot8_i32_i4 v8, v47, v89, v8
	v_dot8_i32_i4 v9, v47, v90, v9
	s_waitcnt lgkmcnt(0)
	v_add_u32_e32 v105, v105, v113
	v_permlane32_swap_b32 v106, v114
	v_lshl_add_u32 v115, v8, 4, v9
	v_dot8_i32_i4 v8, v44, v1, 0
	v_dot8_i32_i4 v9, v44, v88, 0
	v_dot8_i32_i4 v8, v45, v89, v8
	v_dot8_i32_i4 v9, v45, v90, v9
	s_waitcnt lgkmcnt(0)
	v_add_u32_e32 v106, v106, v114
	v_permlane32_swap_b32 v107, v115
	v_lshl_add_u32 v116, v8, 4, v9
	v_dot8_i32_i4 v8, v42, v1, 0
	v_dot8_i32_i4 v9, v42, v88, 0
	v_dot8_i32_i4 v8, v43, v89, v8
	v_dot8_i32_i4 v9, v43, v90, v9
	s_waitcnt lgkmcnt(0)
	v_add_u32_e32 v107, v107, v115
	v_permlane32_swap_b32 v108, v116
	v_lshl_add_u32 v117, v8, 4, v9
	v_dot8_i32_i4 v8, v40, v1, 0
	v_dot8_i32_i4 v9, v40, v88, 0
	v_dot8_i32_i4 v8, v41, v89, v8
	v_dot8_i32_i4 v9, v41, v90, v9
	s_waitcnt lgkmcnt(0)
	v_add_u32_e32 v108, v108, v116
	v_permlane32_swap_b32 v109, v117
	v_lshl_add_u32 v118, v8, 4, v9
	s_waitcnt lgkmcnt(0)
	v_add_u32_e32 v109, v109, v117
	v_permlane32_swap_b32 v110, v118
	v_readlane_b32 s50, v92, 12
	s_lshl_b64 s[16:17], s[16:17], 9
	s_ashr_i32 s19, s18, 31
	s_waitcnt lgkmcnt(0)
	v_add_u32_e32 v110, v110, v118
	v_permlane16_swap_b32 v87, v107
	v_readlane_b32 s20, v92, 4
	s_add_u32 s66, s28, s62
	s_addc_u32 s67, s29, s63
	global_load_dwordx2 v[24:25], v121, s[66:67]
	s_add_u32 s66, s30, s62
	s_addc_u32 s67, s31, s63
	global_load_dwordx2 v[38:39], v121, s[66:67]
	s_waitcnt lgkmcnt(0)
	v_add_u32_e32 v87, v87, v107
	v_permlane16_swap_b32 v104, v108
	s_lshl_b64 s[38:39], s[38:39], 9
	s_ashr_i32 s51, s50, 31
	v_readlane_b32 s52, v92, 13
	s_waitcnt lgkmcnt(0)
	v_add_u32_e32 v104, v104, v108
	v_permlane16_swap_b32 v105, v109
	s_lshl_b64 s[18:19], s[18:19], 9
	s_ashr_i32 s21, s20, 31
	v_readlane_b32 s22, v92, 5
	s_waitcnt lgkmcnt(0)
	v_add_u32_e32 v105, v105, v109
	v_permlane16_swap_b32 v106, v110
	s_add_u32 s66, s34, s62
	s_addc_u32 s67, s35, s63
	global_load_dwordx2 v[50:51], v121, s[66:67]
	s_lshl_b64 s[50:51], s[50:51], 9
	s_ashr_i32 s53, s52, 31
	s_waitcnt lgkmcnt(0)
	v_add_u32_e32 v106, v106, v110
	v_cndmask_b32_e64 v107, v87, v105, s[44:45]
	v_cndmask_b32_e64 v87, v105, v87, s[44:45]
	s_nop 0
	v_readlane_b32 s54, v92, 14
	s_lshl_b64 s[20:21], s[20:21], 9
	s_ashr_i32 s23, s22, 31
	v_readlane_b32 s24, v92, 6
	s_waitcnt lgkmcnt(0)
	v_add_u32_dpp v87, v107, v87 row_ror:8 row_mask:0xf bank_mask:0xf
	v_cndmask_b32_e64 v105, v104, v106, s[44:45]
	s_nop 1
	v_cndmask_b32_e64 v104, v106, v104, s[44:45]
	s_lshl_b64 s[52:53], s[52:53], 9
	s_ashr_i32 s55, s54, 31
	v_readlane_b32 s56, v92, 15
	s_waitcnt lgkmcnt(0)
	v_add_u32_dpp v104, v105, v104 row_ror:8 row_mask:0xf bank_mask:0xf
	v_cndmask_b32_e64 v105, v87, v104, s[46:47]
	v_cndmask_b32_e64 v87, v104, v87, s[46:47]
	s_nop 0
	v_mov_b32_dpp v104, v105 row_half_mirror row_mask:0xf bank_mask:0xf
	s_nop 1
	s_lshl_b64 s[22:23], s[22:23], 9
	s_ashr_i32 s25, s24, 31
	v_readlane_b32 s26, v92, 7
	s_lshl_b64 s[54:55], s[54:55], 9
	s_waitcnt lgkmcnt(0)
	v_add_u32_dpp v87, v104, v87 quad_perm:[3,2,1,0] row_mask:0xf bank_mask:0xf
	s_nop 1
	s_ashr_i32 s57, s56, 31
	s_lshl_b64 s[24:25], s[24:25], 9
	s_ashr_i32 s27, s26, 31
	s_lshl_b64 s[56:57], s[56:57], 9
	s_waitcnt lgkmcnt(0)
	v_add_u32_dpp v87, v87, v87 quad_perm:[2,3,0,1] row_mask:0xf bank_mask:0xf
	s_nop 1
	s_lshl_b64 s[26:27], s[26:27], 9
	s_waitcnt lgkmcnt(0)
	v_add_u32_dpp v87, v87, v87 quad_perm:[1,0,3,2] row_mask:0xf bank_mask:0xf
	s_waitcnt vmcnt(4)
	v_mul_f32_e32 v85, v91, v85
	v_cvt_f32_i32_e32 v87, v87
	v_add_f32_e32 v87, v95, v87
	v_mul_f32_e32 v85, v85, v87
	v_mul_f32_e32 v87, 0x3d372713, v85
	v_mul_f32_e32 v87, v85, v87
	v_fma_f32 v87, v85, v87, v85
	v_mul_f32_e32 v87, 0x3fcc422a, v87
	v_mul_f32_e32 v87, 0xbfb8aa3b, v87
	v_exp_f32_e32 v87, v87
	s_nop 0
	v_add_f32_e32 v87, 1.0, v87
	v_rcp_f32_e32 v87, v87
	s_nop 0
	v_pk_mul_f32 v[84:85], v[84:85], v[86:87]
	s_waitcnt vmcnt(21)
	v_alignbit_b32 v224, v82, v82, 4
	v_pk_mul_f32 v[84:85], v[84:85], v[84:85] op_sel:[0,1] op_sel_hi:[1,0]
	v_cvt_f16_f32_e32 v120, v84
	s_setprio 0
	s_add_u32 s66, s38, s62
	s_addc_u32 s67, s39, s63
	global_load_dwordx2 v[48:49], v121, s[66:67]
	s_add_u32 s66, s50, s62
	s_addc_u32 s67, s51, s63
	global_load_dwordx2 v[46:47], v121, s[66:67]
	s_add_u32 s66, s52, s62
	s_addc_u32 s67, s53, s63
	global_load_dwordx2 v[44:45], v121, s[66:67]
	s_add_u32 s66, s54, s62
	s_addc_u32 s67, s55, s63
	global_load_dwordx2 v[42:43], v121, s[66:67]
	s_add_u32 s66, s56, s62
	s_addc_u32 s67, s57, s63
	global_load_dwordx2 v[40:41], v121, s[66:67]
	s_add_u32 s66, s12, s62
	s_addc_u32 s67, s13, s63
	global_load_dwordx2 v[8:9], v121, s[66:67]
	s_add_u32 s66, s14, s62
	s_addc_u32 s67, s15, s63
	global_load_dwordx2 v[10:11], v121, s[66:67]
	s_add_u32 s66, s16, s62
	s_addc_u32 s67, s17, s63
	global_load_dwordx2 v[12:13], v121, s[66:67]
	s_add_u32 s66, s18, s62
	s_addc_u32 s67, s19, s63
	global_load_dwordx2 v[14:15], v121, s[66:67]
	s_add_u32 s66, s20, s62
	s_addc_u32 s67, s21, s63
	global_load_dwordx2 v[16:17], v121, s[66:67]
	s_add_u32 s66, s22, s62
	s_addc_u32 s67, s23, s63
	global_load_dwordx2 v[18:19], v121, s[66:67]
	s_add_u32 s66, s24, s62
	s_addc_u32 s67, s25, s63
	global_load_dwordx2 v[20:21], v121, s[66:67]
	s_add_u32 s66, s26, s62
	s_addc_u32 s67, s27, s63
	global_load_dwordx2 v[22:23], v121, s[66:67]
	v_and_b32_e32 v86, 0x7070707, v82
	v_readlane_b32 s36, v120, 0
	v_and_b32_e32 v87, 0x7070707, v224
	v_perm_b32 v86, s2, v205, v86
	v_perm_b32 v87, s2, v205, v87
	v_and_or_b32 v86, v82, s4, v86
	v_and_or_b32 v82, v224, s4, v87
	v_perm_b32 v87, v82, v86, s5
	v_perm_b32 v104, v82, v86, s33
	v_perm_b32 v105, v82, v86, s0
	v_perm_b32 v82, v82, v86, s1
	v_pk_fma_f16 v86, v87, s36, v103 op_sel_hi:[1,0,1]
	v_pk_fma_f16 v87, v104, s36, v102 op_sel_hi:[1,0,1]
	v_alignbit_b32 v225, v83, v83, 4
	v_pk_fma_f16 v82, v82, s36, v100 op_sel_hi:[1,0,1]
	v_and_b32_e32 v100, 0x7070707, v83
	v_and_b32_e32 v102, 0x7070707, v225
	v_perm_b32 v100, s2, v205, v100
	v_perm_b32 v102, s2, v205, v102
	v_and_or_b32 v100, v83, s4, v100
	v_and_or_b32 v83, v225, s4, v102
	v_perm_b32 v102, v83, v100, s5
	v_perm_b32 v103, v83, v100, s33
	v_perm_b32 v104, v83, v100, s0
	v_perm_b32 v83, v83, v100, s1
	v_readlane_b32 s59, v120, 4
	s_waitcnt vmcnt(33)
	v_alignbit_b32 v224, v80, v80, 4
	v_pk_fma_f16 v101, v105, s36, v101 op_sel_hi:[1,0,1]
	v_pk_fma_f16 v99, v102, s36, v99 op_sel_hi:[1,0,1]
	v_pk_fma_f16 v98, v103, s36, v98 op_sel_hi:[1,0,1]
	v_pk_fma_f16 v97, v104, s36, v97 op_sel_hi:[1,0,1]
	v_pk_fma_f16 v83, v83, s36, v96 op_sel_hi:[1,0,1]
	v_and_b32_e32 v96, 0x7070707, v80
	v_and_b32_e32 v100, 0x7070707, v224
	v_perm_b32 v96, s2, v205, v96
	v_perm_b32 v100, s2, v205, v100
	v_and_or_b32 v96, v80, s4, v96
	v_and_or_b32 v80, v224, s4, v100
	v_perm_b32 v100, v80, v96, s5
	v_perm_b32 v102, v80, v96, s33
	v_perm_b32 v103, v80, v96, s0
	v_perm_b32 v80, v80, v96, s1
	v_pk_fma_f16 v86, v100, s59, v86 op_sel_hi:[1,0,1]
	v_alignbit_b32 v225, v81, v81, 4
	v_pk_fma_f16 v80, v80, s59, v82 op_sel_hi:[1,0,1]
	v_and_b32_e32 v82, 0x7070707, v81
	v_and_b32_e32 v100, 0x7070707, v225
	v_pk_fma_f16 v96, v103, s59, v101 op_sel_hi:[1,0,1]
	v_perm_b32 v82, s2, v205, v82
	v_perm_b32 v100, s2, v205, v100
	v_and_or_b32 v82, v81, s4, v82
	v_and_or_b32 v81, v225, s4, v100
	v_perm_b32 v100, v81, v82, s5
	v_pk_fma_f16 v87, v102, s59, v87 op_sel_hi:[1,0,1]
	v_perm_b32 v101, v81, v82, s33
	v_perm_b32 v102, v81, v82, s0
	v_perm_b32 v81, v81, v82, s1
	v_pk_fma_f16 v82, v100, s59, v99 op_sel_hi:[1,0,1]
	v_readlane_b32 s60, v120, 8
	s_waitcnt vmcnt(32)
	v_alignbit_b32 v224, v78, v78, 4
	v_pk_fma_f16 v98, v101, s59, v98 op_sel_hi:[1,0,1]
	v_pk_fma_f16 v97, v102, s59, v97 op_sel_hi:[1,0,1]
	v_pk_fma_f16 v81, v81, s59, v83 op_sel_hi:[1,0,1]
	v_and_b32_e32 v85, 0x7070707, v78
	v_and_b32_e32 v99, 0x7070707, v224
	v_perm_b32 v85, s2, v205, v85
	v_perm_b32 v99, s2, v205, v99
	v_and_or_b32 v85, v78, s4, v85
	v_and_or_b32 v78, v224, s4, v99
	v_perm_b32 v99, v78, v85, s5
	v_perm_b32 v100, v78, v85, s33
	v_perm_b32 v101, v78, v85, s0
	v_perm_b32 v78, v78, v85, s1
	v_pk_fma_f16 v85, v99, s60, v86 op_sel_hi:[1,0,1]
	v_pk_fma_f16 v86, v100, s60, v87 op_sel_hi:[1,0,1]
	v_pk_fma_f16 v87, v101, s60, v96 op_sel_hi:[1,0,1]
	v_alignbit_b32 v225, v79, v79, 4
	v_pk_fma_f16 v78, v78, s60, v80 op_sel_hi:[1,0,1]
	v_and_b32_e32 v80, 0x7070707, v79
	v_and_b32_e32 v96, 0x7070707, v225
	v_perm_b32 v80, s2, v205, v80
	v_perm_b32 v96, s2, v205, v96
	v_and_or_b32 v80, v79, s4, v80
	v_and_or_b32 v79, v225, s4, v96
	v_perm_b32 v96, v79, v80, s5
	v_perm_b32 v100, v79, v80, s0
	v_perm_b32 v99, v79, v80, s33
	v_perm_b32 v79, v79, v80, s1
	v_pk_fma_f16 v80, v96, s60, v82 op_sel_hi:[1,0,1]
	v_pk_fma_f16 v96, v100, s60, v97 op_sel_hi:[1,0,1]
	v_readlane_b32 s36, v120, 12
	s_waitcnt vmcnt(31)
	v_alignbit_b32 v224, v76, v76, 4
	v_pk_fma_f16 v82, v99, s60, v98 op_sel_hi:[1,0,1]
	v_pk_fma_f16 v79, v79, s60, v81 op_sel_hi:[1,0,1]
	v_and_b32_e32 v83, 0x7070707, v76
	v_and_b32_e32 v97, 0x7070707, v224
	v_perm_b32 v83, s2, v205, v83
	v_perm_b32 v97, s2, v205, v97
	v_and_or_b32 v83, v76, s4, v83
	v_and_or_b32 v76, v224, s4, v97
	v_perm_b32 v97, v76, v83, s5
	v_perm_b32 v98, v76, v83, s33
	v_perm_b32 v99, v76, v83, s0
	v_perm_b32 v76, v76, v83, s1
	v_pk_fma_f16 v83, v97, s36, v85 op_sel_hi:[1,0,1]
	v_pk_fma_f16 v85, v98, s36, v86 op_sel_hi:[1,0,1]
	v_pk_fma_f16 v86, v99, s36, v87 op_sel_hi:[1,0,1]
	v_alignbit_b32 v225, v77, v77, 4
	v_pk_fma_f16 v76, v76, s36, v78 op_sel_hi:[1,0,1]
	v_and_b32_e32 v78, 0x7070707, v77
	v_and_b32_e32 v87, 0x7070707, v225
	v_perm_b32 v78, s2, v205, v78
	v_perm_b32 v87, s2, v205, v87
	v_and_or_b32 v78, v77, s4, v78
	v_and_or_b32 v77, v225, s4, v87
	v_perm_b32 v87, v77, v78, s5
	v_perm_b32 v97, v77, v78, s33
	v_perm_b32 v98, v77, v78, s0
	v_perm_b32 v77, v77, v78, s1
	v_pk_fma_f16 v78, v87, s36, v80 op_sel_hi:[1,0,1]
	v_readlane_b32 s59, v120, 16
	s_waitcnt vmcnt(30)
	v_alignbit_b32 v224, v74, v74, 4
	v_pk_fma_f16 v80, v97, s36, v82 op_sel_hi:[1,0,1]
	v_pk_fma_f16 v82, v98, s36, v96 op_sel_hi:[1,0,1]
	v_pk_fma_f16 v77, v77, s36, v79 op_sel_hi:[1,0,1]
	v_and_b32_e32 v81, 0x7070707, v74
	v_and_b32_e32 v87, 0x7070707, v224
	v_perm_b32 v81, s2, v205, v81
	v_perm_b32 v87, s2, v205, v87
	v_and_or_b32 v81, v74, s4, v81
	v_and_or_b32 v74, v224, s4, v87
	v_perm_b32 v87, v74, v81, s5
	v_perm_b32 v96, v74, v81, s33
	v_perm_b32 v97, v74, v81, s0
	v_perm_b32 v74, v74, v81, s1
	v_pk_fma_f16 v81, v87, s59, v83 op_sel_hi:[1,0,1]
	v_pk_fma_f16 v83, v96, s59, v85 op_sel_hi:[1,0,1]
	v_pk_fma_f16 v85, v97, s59, v86 op_sel_hi:[1,0,1]
	v_alignbit_b32 v225, v75, v75, 4
	v_pk_fma_f16 v74, v74, s59, v76 op_sel_hi:[1,0,1]
	v_and_b32_e32 v76, 0x7070707, v75
	v_and_b32_e32 v86, 0x7070707, v225
	v_perm_b32 v76, s2, v205, v76
	v_perm_b32 v86, s2, v205, v86
	v_and_or_b32 v76, v75, s4, v76
	v_and_or_b32 v75, v225, s4, v86
	v_perm_b32 v86, v75, v76, s5
	v_perm_b32 v87, v75, v76, s33
	v_perm_b32 v96, v75, v76, s0
	v_perm_b32 v75, v75, v76, s1
	v_pk_fma_f16 v76, v86, s59, v78 op_sel_hi:[1,0,1]
	v_pk_fma_f16 v78, v87, s59, v80 op_sel_hi:[1,0,1]
	v_pk_fma_f16 v80, v96, s59, v82 op_sel_hi:[1,0,1]
	v_readlane_b32 s60, v120, 20
	s_waitcnt vmcnt(29)
	v_alignbit_b32 v224, v70, v70, 4
	v_pk_fma_f16 v75, v75, s59, v77 op_sel_hi:[1,0,1]
	v_and_b32_e32 v79, 0x7070707, v70
	v_and_b32_e32 v82, 0x7070707, v224
	v_perm_b32 v79, s2, v205, v79
	v_perm_b32 v82, s2, v205, v82
	v_and_or_b32 v79, v70, s4, v79
	v_and_or_b32 v70, v224, s4, v82
	v_perm_b32 v82, v70, v79, s5
	v_perm_b32 v86, v70, v79, s33
	v_perm_b32 v87, v70, v79, s0
	v_perm_b32 v70, v70, v79, s1
	v_pk_fma_f16 v79, v82, s60, v81 op_sel_hi:[1,0,1]
	v_pk_fma_f16 v81, v86, s60, v83 op_sel_hi:[1,0,1]
	v_alignbit_b32 v225, v71, v71, 4
	v_pk_fma_f16 v70, v70, s60, v74 op_sel_hi:[1,0,1]
	v_and_b32_e32 v74, 0x7070707, v71
	v_and_b32_e32 v83, 0x7070707, v225
	v_pk_fma_f16 v82, v87, s60, v85 op_sel_hi:[1,0,1]
	v_perm_b32 v74, s2, v205, v74
	v_perm_b32 v83, s2, v205, v83
	v_and_or_b32 v74, v71, s4, v74
	v_and_or_b32 v71, v225, s4, v83
	v_perm_b32 v83, v71, v74, s5
	v_perm_b32 v85, v71, v74, s33
	v_perm_b32 v86, v71, v74, s0
	v_perm_b32 v71, v71, v74, s1
	v_pk_fma_f16 v74, v83, s60, v76 op_sel_hi:[1,0,1]
	v_pk_fma_f16 v76, v85, s60, v78 op_sel_hi:[1,0,1]
	v_pk_fma_f16 v78, v86, s60, v80 op_sel_hi:[1,0,1]
	v_readlane_b32 s36, v120, 24
	s_waitcnt vmcnt(28)
	v_alignbit_b32 v224, v68, v68, 4
	v_pk_fma_f16 v71, v71, s60, v75 op_sel_hi:[1,0,1]
	v_and_b32_e32 v77, 0x7070707, v68
	v_and_b32_e32 v80, 0x7070707, v224
	v_perm_b32 v77, s2, v205, v77
	v_perm_b32 v80, s2, v205, v80
	v_and_or_b32 v77, v68, s4, v77
	v_and_or_b32 v68, v224, s4, v80
	v_perm_b32 v80, v68, v77, s5
	v_perm_b32 v83, v68, v77, s33
	v_perm_b32 v85, v68, v77, s0
	v_perm_b32 v68, v68, v77, s1
	v_pk_fma_f16 v77, v80, s36, v79 op_sel_hi:[1,0,1]
	v_pk_fma_f16 v79, v83, s36, v81 op_sel_hi:[1,0,1]
	v_alignbit_b32 v225, v69, v69, 4
	v_pk_fma_f16 v68, v68, s36, v70 op_sel_hi:[1,0,1]
	v_and_b32_e32 v70, 0x7070707, v69
	v_and_b32_e32 v81, 0x7070707, v225
	v_pk_fma_f16 v80, v85, s36, v82 op_sel_hi:[1,0,1]
	v_perm_b32 v70, s2, v205, v70
	v_perm_b32 v81, s2, v205, v81
	v_and_or_b32 v70, v69, s4, v70
	v_and_or_b32 v69, v225, s4, v81
	v_perm_b32 v81, v69, v70, s5
	v_perm_b32 v82, v69, v70, s33
	v_perm_b32 v83, v69, v70, s0
	v_perm_b32 v69, v69, v70, s1
	v_pk_fma_f16 v70, v81, s36, v74 op_sel_hi:[1,0,1]
	v_pk_fma_f16 v74, v82, s36, v76 op_sel_hi:[1,0,1]
	v_pk_fma_f16 v76, v83, s36, v78 op_sel_hi:[1,0,1]
	v_readlane_b32 s59, v120, 28
	s_waitcnt vmcnt(25)
	v_alignbit_b32 v224, v64, v64, 4
	v_pk_fma_f16 v69, v69, s36, v71 op_sel_hi:[1,0,1]
	v_and_b32_e32 v75, 0x7070707, v64
	v_and_b32_e32 v78, 0x7070707, v224
	v_perm_b32 v75, s2, v205, v75
	v_perm_b32 v78, s2, v205, v78
	v_and_or_b32 v75, v64, s4, v75
	v_and_or_b32 v64, v224, s4, v78
	v_perm_b32 v78, v64, v75, s5
	v_perm_b32 v81, v64, v75, s33
	v_perm_b32 v82, v64, v75, s0
	v_perm_b32 v64, v64, v75, s1
	v_pk_fma_f16 v75, v78, s59, v77 op_sel_hi:[1,0,1]
	v_pk_fma_f16 v77, v81, s59, v79 op_sel_hi:[1,0,1]
	v_alignbit_b32 v225, v65, v65, 4
	v_pk_fma_f16 v64, v64, s59, v68 op_sel_hi:[1,0,1]
	v_and_b32_e32 v68, 0x7070707, v65
	v_and_b32_e32 v79, 0x7070707, v225
	v_pk_fma_f16 v78, v82, s59, v80 op_sel_hi:[1,0,1]
	s_add_u32 s66, s12, s64
	s_addc_u32 s67, s13, s65
	global_load_dwordx2 v[82:83], v121, s[66:67]
	v_perm_b32 v68, s2, v205, v68
	v_perm_b32 v79, s2, v205, v79
	v_and_or_b32 v68, v65, s4, v68
	v_and_or_b32 v65, v225, s4, v79
	v_perm_b32 v79, v65, v68, s5
	v_perm_b32 v80, v65, v68, s33
	v_perm_b32 v81, v65, v68, s0
	v_perm_b32 v65, v65, v68, s1
	v_pk_fma_f16 v68, v79, s59, v70 op_sel_hi:[1,0,1]
	v_pk_fma_f16 v70, v80, s59, v74 op_sel_hi:[1,0,1]
	v_pk_fma_f16 v74, v81, s59, v76 op_sel_hi:[1,0,1]
	v_readlane_b32 s60, v120, 32
	s_waitcnt vmcnt(25)
	v_alignbit_b32 v224, v62, v62, 4
	v_pk_fma_f16 v65, v65, s59, v69 op_sel_hi:[1,0,1]
	v_and_b32_e32 v71, 0x7070707, v62
	v_and_b32_e32 v76, 0x7070707, v224
	v_perm_b32 v71, s2, v205, v71
	v_perm_b32 v76, s2, v205, v76
	v_and_or_b32 v71, v62, s4, v71
	v_and_or_b32 v62, v224, s4, v76
	v_perm_b32 v76, v62, v71, s5
	v_perm_b32 v79, v62, v71, s33
	v_perm_b32 v80, v62, v71, s0
	v_perm_b32 v62, v62, v71, s1
	v_pk_fma_f16 v71, v76, s60, v75 op_sel_hi:[1,0,1]
	v_pk_fma_f16 v75, v79, s60, v77 op_sel_hi:[1,0,1]
	v_alignbit_b32 v225, v63, v63, 4
	v_pk_fma_f16 v62, v62, s60, v64 op_sel_hi:[1,0,1]
	v_and_b32_e32 v64, 0x7070707, v63
	v_and_b32_e32 v77, 0x7070707, v225
	v_pk_fma_f16 v76, v80, s60, v78 op_sel_hi:[1,0,1]
	s_add_u32 s66, s14, s64
	s_addc_u32 s67, s15, s65
	global_load_dwordx2 v[80:81], v121, s[66:67]
	v_perm_b32 v64, s2, v205, v64
	v_perm_b32 v77, s2, v205, v77
	v_and_or_b32 v64, v63, s4, v64
	v_and_or_b32 v63, v225, s4, v77
	v_perm_b32 v77, v63, v64, s5
	v_perm_b32 v78, v63, v64, s33
	v_perm_b32 v79, v63, v64, s0
	v_perm_b32 v63, v63, v64, s1
	v_pk_fma_f16 v64, v77, s60, v68 op_sel_hi:[1,0,1]
	v_pk_fma_f16 v68, v78, s60, v70 op_sel_hi:[1,0,1]
	v_pk_fma_f16 v70, v79, s60, v74 op_sel_hi:[1,0,1]
	v_readlane_b32 s36, v120, 36
	s_waitcnt vmcnt(29)
	v_alignbit_b32 v224, v66, v66, 4
	v_pk_fma_f16 v63, v63, s60, v65 op_sel_hi:[1,0,1]
	v_and_b32_e32 v69, 0x7070707, v66
	v_and_b32_e32 v74, 0x7070707, v224
	v_perm_b32 v69, s2, v205, v69
	v_perm_b32 v74, s2, v205, v74
	v_and_or_b32 v69, v66, s4, v69
	v_and_or_b32 v66, v224, s4, v74
	v_perm_b32 v74, v66, v69, s5
	v_perm_b32 v77, v66, v69, s33
	v_perm_b32 v78, v66, v69, s0
	v_perm_b32 v66, v66, v69, s1
	v_pk_fma_f16 v69, v74, s36, v71 op_sel_hi:[1,0,1]
	v_pk_fma_f16 v71, v77, s36, v75 op_sel_hi:[1,0,1]
	v_alignbit_b32 v225, v67, v67, 4
	v_pk_fma_f16 v62, v66, s36, v62 op_sel_hi:[1,0,1]
	v_and_b32_e32 v66, 0x7070707, v67
	v_and_b32_e32 v75, 0x7070707, v225
	v_pk_fma_f16 v74, v78, s36, v76 op_sel_hi:[1,0,1]
	s_add_u32 s66, s16, s64
	s_addc_u32 s67, s17, s65
	global_load_dwordx2 v[78:79], v121, s[66:67]
	v_perm_b32 v66, s2, v205, v66
	v_perm_b32 v75, s2, v205, v75
	v_and_or_b32 v66, v67, s4, v66
	v_and_or_b32 v67, v225, s4, v75
	v_perm_b32 v76, v67, v66, s33
	v_perm_b32 v77, v67, v66, s0
	v_perm_b32 v75, v67, v66, s5
	v_perm_b32 v66, v67, v66, s1
	v_pk_fma_f16 v67, v76, s36, v68 op_sel_hi:[1,0,1]
	v_pk_fma_f16 v68, v77, s36, v70 op_sel_hi:[1,0,1]
	v_readlane_b32 s59, v120, 40
	s_waitcnt vmcnt(26)
	v_alignbit_b32 v224, v60, v60, 4
	v_pk_fma_f16 v64, v75, s36, v64 op_sel_hi:[1,0,1]
	v_pk_fma_f16 v63, v66, s36, v63 op_sel_hi:[1,0,1]
	v_and_b32_e32 v66, 0x7070707, v60
	v_and_b32_e32 v70, 0x7070707, v224
	v_perm_b32 v66, s2, v205, v66
	v_perm_b32 v70, s2, v205, v70
	v_and_or_b32 v66, v60, s4, v66
	v_and_or_b32 v60, v224, s4, v70
	v_perm_b32 v70, v60, v66, s5
	v_perm_b32 v75, v60, v66, s33
	v_perm_b32 v76, v60, v66, s0
	v_perm_b32 v60, v60, v66, s1
	v_pk_fma_f16 v66, v70, s59, v69 op_sel_hi:[1,0,1]
	v_pk_fma_f16 v69, v75, s59, v71 op_sel_hi:[1,0,1]
	v_alignbit_b32 v225, v61, v61, 4
	v_pk_fma_f16 v60, v60, s59, v62 op_sel_hi:[1,0,1]
	v_and_b32_e32 v62, 0x7070707, v61
	v_and_b32_e32 v71, 0x7070707, v225
	v_pk_fma_f16 v70, v76, s59, v74 op_sel_hi:[1,0,1]
	s_add_u32 s66, s18, s64
	s_addc_u32 s67, s19, s65
	global_load_dwordx2 v[76:77], v121, s[66:67]
	v_perm_b32 v62, s2, v205, v62
	v_perm_b32 v71, s2, v205, v71
	v_and_or_b32 v62, v61, s4, v62
	v_and_or_b32 v61, v225, s4, v71
	v_perm_b32 v71, v61, v62, s5
	v_perm_b32 v74, v61, v62, s33
	v_perm_b32 v75, v61, v62, s0
	v_perm_b32 v61, v61, v62, s1
	v_pk_fma_f16 v62, v71, s59, v64 op_sel_hi:[1,0,1]
	v_pk_fma_f16 v64, v74, s59, v67 op_sel_hi:[1,0,1]
	v_pk_fma_f16 v67, v75, s59, v68 op_sel_hi:[1,0,1]
	v_readlane_b32 s60, v120, 44
	s_waitcnt vmcnt(26)
	v_alignbit_b32 v224, v58, v58, 4
	v_pk_fma_f16 v61, v61, s59, v63 op_sel_hi:[1,0,1]
	v_and_b32_e32 v65, 0x7070707, v58
	v_and_b32_e32 v68, 0x7070707, v224
	v_perm_b32 v65, s2, v205, v65
	v_perm_b32 v68, s2, v205, v68
	v_and_or_b32 v65, v58, s4, v65
	v_and_or_b32 v58, v224, s4, v68
	v_perm_b32 v68, v58, v65, s5
	v_perm_b32 v71, v58, v65, s33
	v_perm_b32 v74, v58, v65, s0
	v_perm_b32 v58, v58, v65, s1
	v_pk_fma_f16 v65, v68, s60, v66 op_sel_hi:[1,0,1]
	v_pk_fma_f16 v66, v71, s60, v69 op_sel_hi:[1,0,1]
	v_alignbit_b32 v225, v59, v59, 4
	v_pk_fma_f16 v58, v58, s60, v60 op_sel_hi:[1,0,1]
	v_and_b32_e32 v60, 0x7070707, v59
	v_and_b32_e32 v69, 0x7070707, v225
	v_pk_fma_f16 v68, v74, s60, v70 op_sel_hi:[1,0,1]
	s_add_u32 s66, s20, s64
	s_addc_u32 s67, s21, s65
	global_load_dwordx2 v[74:75], v121, s[66:67]
	v_perm_b32 v60, s2, v205, v60
	v_perm_b32 v69, s2, v205, v69
	v_and_or_b32 v60, v59, s4, v60
	v_and_or_b32 v59, v225, s4, v69
	v_perm_b32 v69, v59, v60, s5
	v_perm_b32 v70, v59, v60, s33
	v_perm_b32 v71, v59, v60, s0
	v_perm_b32 v59, v59, v60, s1
	v_pk_fma_f16 v60, v69, s60, v62 op_sel_hi:[1,0,1]
	v_pk_fma_f16 v62, v70, s60, v64 op_sel_hi:[1,0,1]
	v_pk_fma_f16 v64, v71, s60, v67 op_sel_hi:[1,0,1]
	v_readlane_b32 s36, v120, 48
	s_waitcnt vmcnt(26)
	v_alignbit_b32 v224, v56, v56, 4
	v_pk_fma_f16 v59, v59, s60, v61 op_sel_hi:[1,0,1]
	v_and_b32_e32 v63, 0x7070707, v56
	v_and_b32_e32 v67, 0x7070707, v224
	v_perm_b32 v63, s2, v205, v63
	v_perm_b32 v67, s2, v205, v67
	v_and_or_b32 v63, v56, s4, v63
	v_and_or_b32 v56, v224, s4, v67
	v_perm_b32 v67, v56, v63, s5
	v_perm_b32 v69, v56, v63, s33
	v_perm_b32 v70, v56, v63, s0
	v_perm_b32 v56, v56, v63, s1
	v_pk_fma_f16 v63, v67, s36, v65 op_sel_hi:[1,0,1]
	v_alignbit_b32 v225, v57, v57, 4
	v_pk_fma_f16 v56, v56, s36, v58 op_sel_hi:[1,0,1]
	v_and_b32_e32 v58, 0x7070707, v57
	v_and_b32_e32 v67, 0x7070707, v225
	v_pk_fma_f16 v65, v69, s36, v66 op_sel_hi:[1,0,1]
	v_pk_fma_f16 v66, v70, s36, v68 op_sel_hi:[1,0,1]
	s_add_u32 s66, s22, s64
	s_addc_u32 s67, s23, s65
	global_load_dwordx2 v[70:71], v121, s[66:67]
	v_perm_b32 v58, s2, v205, v58
	v_perm_b32 v67, s2, v205, v67
	v_and_or_b32 v58, v57, s4, v58
	v_and_or_b32 v57, v225, s4, v67
	v_perm_b32 v67, v57, v58, s5
	v_perm_b32 v68, v57, v58, s33
	v_perm_b32 v69, v57, v58, s0
	v_perm_b32 v57, v57, v58, s1
	v_pk_fma_f16 v58, v67, s36, v60 op_sel_hi:[1,0,1]
	v_pk_fma_f16 v60, v68, s36, v62 op_sel_hi:[1,0,1]
	v_pk_fma_f16 v62, v69, s36, v64 op_sel_hi:[1,0,1]
	v_readlane_b32 s59, v120, 52
	s_waitcnt vmcnt(26)
	v_alignbit_b32 v224, v54, v54, 4
	v_pk_fma_f16 v57, v57, s36, v59 op_sel_hi:[1,0,1]
	v_and_b32_e32 v61, 0x7070707, v54
	v_and_b32_e32 v64, 0x7070707, v224
	v_perm_b32 v61, s2, v205, v61
	v_perm_b32 v64, s2, v205, v64
	v_and_or_b32 v61, v54, s4, v61
	v_and_or_b32 v54, v224, s4, v64
	v_perm_b32 v64, v54, v61, s5
	v_perm_b32 v67, v54, v61, s33
	v_perm_b32 v68, v54, v61, s0
	v_perm_b32 v54, v54, v61, s1
	v_pk_fma_f16 v61, v64, s59, v63 op_sel_hi:[1,0,1]
	v_pk_fma_f16 v63, v67, s59, v65 op_sel_hi:[1,0,1]
	v_alignbit_b32 v225, v55, v55, 4
	v_pk_fma_f16 v54, v54, s59, v56 op_sel_hi:[1,0,1]
	v_and_b32_e32 v56, 0x7070707, v55
	v_and_b32_e32 v65, 0x7070707, v225
	v_pk_fma_f16 v64, v68, s59, v66 op_sel_hi:[1,0,1]
	s_add_u32 s66, s24, s64
	s_addc_u32 s67, s25, s65
	global_load_dwordx2 v[68:69], v121, s[66:67]
	v_perm_b32 v56, s2, v205, v56
	v_perm_b32 v65, s2, v205, v65
	v_and_or_b32 v56, v55, s4, v56
	v_and_or_b32 v55, v225, s4, v65
	v_perm_b32 v65, v55, v56, s5
	v_perm_b32 v66, v55, v56, s33
	v_perm_b32 v67, v55, v56, s0
	v_perm_b32 v55, v55, v56, s1
	v_pk_fma_f16 v56, v65, s59, v58 op_sel_hi:[1,0,1]
	v_pk_fma_f16 v58, v66, s59, v60 op_sel_hi:[1,0,1]
	v_pk_fma_f16 v60, v67, s59, v62 op_sel_hi:[1,0,1]
	v_readlane_b32 s60, v120, 56
	s_waitcnt vmcnt(26)
	v_alignbit_b32 v224, v52, v52, 4
	v_pk_fma_f16 v55, v55, s59, v57 op_sel_hi:[1,0,1]
	v_and_b32_e32 v59, 0x7070707, v52
	v_and_b32_e32 v62, 0x7070707, v224
	v_perm_b32 v59, s2, v205, v59
	v_perm_b32 v62, s2, v205, v62
	v_and_or_b32 v59, v52, s4, v59
	v_and_or_b32 v52, v224, s4, v62
	v_perm_b32 v62, v52, v59, s5
	v_perm_b32 v65, v52, v59, s33
	v_perm_b32 v66, v52, v59, s0
	v_perm_b32 v52, v52, v59, s1
	v_pk_fma_f16 v59, v62, s60, v61 op_sel_hi:[1,0,1]
	v_pk_fma_f16 v61, v65, s60, v63 op_sel_hi:[1,0,1]
	v_alignbit_b32 v225, v53, v53, 4
	v_pk_fma_f16 v52, v52, s60, v54 op_sel_hi:[1,0,1]
	v_and_b32_e32 v54, 0x7070707, v53
	v_and_b32_e32 v63, 0x7070707, v225
	v_pk_fma_f16 v62, v66, s60, v64 op_sel_hi:[1,0,1]
	s_add_u32 s66, s30, s64
	s_addc_u32 s67, s31, s65
	global_load_dwordx2 v[66:67], v121, s[66:67]
	v_perm_b32 v54, s2, v205, v54
	v_perm_b32 v63, s2, v205, v63
	v_and_or_b32 v54, v53, s4, v54
	v_and_or_b32 v53, v225, s4, v63
	v_perm_b32 v63, v53, v54, s5
	v_perm_b32 v64, v53, v54, s33
	v_perm_b32 v65, v53, v54, s0
	v_perm_b32 v53, v53, v54, s1
	v_pk_fma_f16 v54, v63, s60, v56 op_sel_hi:[1,0,1]
	v_pk_fma_f16 v56, v64, s60, v58 op_sel_hi:[1,0,1]
	v_pk_fma_f16 v58, v65, s60, v60 op_sel_hi:[1,0,1]
	v_readlane_b32 s36, v120, 60
	s_waitcnt vmcnt(34)
	v_alignbit_b32 v224, v36, v36, 4
	v_pk_fma_f16 v53, v53, s60, v55 op_sel_hi:[1,0,1]
	v_and_b32_e32 v57, 0x7070707, v36
	v_and_b32_e32 v60, 0x7070707, v224
	v_perm_b32 v57, s2, v205, v57
	v_perm_b32 v60, s2, v205, v60
	v_and_or_b32 v57, v36, s4, v57
	v_and_or_b32 v36, v224, s4, v60
	v_perm_b32 v60, v36, v57, s5
	v_perm_b32 v63, v36, v57, s33
	v_perm_b32 v64, v36, v57, s0
	v_perm_b32 v36, v36, v57, s1
	v_pk_fma_f16 v100, v36, s36, v52 op_sel_hi:[1,0,1]
	v_alignbit_b32 v225, v37, v37, 4
	v_and_b32_e32 v36, 0x7070707, v37
	v_and_b32_e32 v52, 0x7070707, v225
	v_perm_b32 v36, s2, v205, v36
	v_perm_b32 v52, s2, v205, v52
	v_and_or_b32 v36, v37, s4, v36
	v_and_or_b32 v37, v225, s4, v52
	v_pk_fma_f16 v103, v60, s36, v59 op_sel_hi:[1,0,1]
	v_perm_b32 v52, v37, v36, s5
	v_perm_b32 v57, v37, v36, s33
	v_perm_b32 v59, v37, v36, s0
	v_perm_b32 v36, v37, v36, s1
	v_pk_fma_f16 v96, v36, s36, v53 op_sel_hi:[1,0,1]
	s_add_u32 s66, s56, s64
	s_addc_u32 s67, s57, s65
	global_load_dwordx2 v[36:37], v121, s[66:67]
	v_pk_fma_f16 v101, v64, s36, v62 op_sel_hi:[1,0,1]
	s_add_u32 s66, s26, s64
	s_addc_u32 s67, s27, s65
	global_load_dwordx2 v[64:65], v121, s[66:67]
	v_pk_fma_f16 v102, v63, s36, v61 op_sel_hi:[1,0,1]
	s_add_u32 s66, s28, s64
	s_addc_u32 s67, s29, s65
	global_load_dwordx2 v[62:63], v121, s[66:67]
	s_add_u32 s66, s34, s64
	s_addc_u32 s67, s35, s65
	global_load_dwordx2 v[60:61], v121, s[66:67]
	v_pk_fma_f16 v97, v59, s36, v58 op_sel_hi:[1,0,1]
	s_add_u32 s66, s38, s64
	s_addc_u32 s67, s39, s65
	global_load_dwordx2 v[58:59], v121, s[66:67]
	v_pk_fma_f16 v98, v57, s36, v56 op_sel_hi:[1,0,1]
	s_add_u32 s66, s50, s64
	s_addc_u32 s67, s51, s65
	global_load_dwordx2 v[56:57], v121, s[66:67]
	v_pk_fma_f16 v99, v52, s36, v54 op_sel_hi:[1,0,1]
	s_add_u32 s66, s52, s64
	s_addc_u32 s67, s53, s65
	global_load_dwordx2 v[54:55], v121, s[66:67]
	s_add_u32 s66, s54, s64
	s_addc_u32 s67, s55, s65
	global_load_dwordx2 v[52:53], v121, s[66:67]
	s_nop 0
	s_nop 0
	s_nop 0
	s_nop 0
	s_nop 0
	s_nop 0
	s_nop 0
	s_cmpk_eq_i32 s58, 0x90
	s_cbranch_scc0 .LBB0_763
	v_lshlrev_b64 v[0:1], 2, v[2:3]
	v_lshl_add_u64 v[2:3], v[28:29], 0, v[0:1]
	v_mov_b32_e32 v104, v208
	v_mov_b32_e32 v105, v209
	v_mov_b32_e32 v106, v210
	v_mov_b32_e32 v107, v211
	v_mov_b32_e32 v108, v212
	v_mov_b32_e32 v109, v213
	v_mov_b32_e32 v110, v214
	v_mov_b32_e32 v111, v215
	v_mov_b32_e32 v86, v216
	v_mov_b32_e32 v87, v217
	v_mov_b32_e32 v88, v218
	v_mov_b32_e32 v89, v219
	v_mov_b32_e32 v112, v220
	v_mov_b32_e32 v113, v221
	v_mov_b32_e32 v114, v222
	v_mov_b32_e32 v115, v223
	v_lshl_add_u64 v[72:73], v[32:33], 0, v[0:1]
	v_cvt_f32_f16_sdwa v1, v103 dst_sel:DWORD dst_unused:UNUSED_PAD src0_sel:WORD_1
	v_cvt_f32_f16_e32 v0, v103
	v_cvt_f32_f16_sdwa v91, v102 dst_sel:DWORD dst_unused:UNUSED_PAD src0_sel:WORD_1
	v_cvt_f32_f16_e32 v90, v102
	v_cvt_f32_f16_sdwa v103, v101 dst_sel:DWORD dst_unused:UNUSED_PAD src0_sel:WORD_1
	v_cvt_f32_f16_e32 v102, v101
	v_cvt_f32_f16_sdwa v101, v100 dst_sel:DWORD dst_unused:UNUSED_PAD src0_sel:WORD_1
	v_cvt_f32_f16_e32 v100, v100
	s_mov_b32 s18, 0x800000
	v_readlane_b32 s12, v255, 5
	v_readlane_b32 s13, v255, 6
	v_pk_add_f32 v[86:87], v[86:87], v[102:103]
	v_pk_add_f32 v[84:85], v[112:113], v[0:1]
	v_mov_b32_e32 v102, v85
	v_mov_b32_e32 v103, v87
	v_pk_add_f32 v[90:91], v[114:115], v[90:91]
	v_pk_add_f32 v[88:89], v[88:89], v[100:101]
	v_mov_b32_e32 v100, v84
	v_mov_b32_e32 v101, v86
	v_pk_mul_f32 v[102:103], v[102:103], v[102:103]
	v_mov_b32_e32 v112, v91
	v_pk_fma_f32 v[100:101], v[100:101], v[100:101], v[102:103]
	v_mov_b32_e32 v102, v90
	v_mov_b32_e32 v103, v88
	v_pk_fma_f32 v[100:101], v[102:103], v[102:103], v[100:101]
	v_cvt_f32_f16_sdwa v103, v99 dst_sel:DWORD dst_unused:UNUSED_PAD src0_sel:WORD_1
	v_cvt_f32_f16_e32 v102, v99
	v_cvt_f32_f16_sdwa v99, v98 dst_sel:DWORD dst_unused:UNUSED_PAD src0_sel:WORD_1
	v_cvt_f32_f16_e32 v98, v98
	v_mov_b32_e32 v113, v89
	v_pk_add_f32 v[102:103], v[108:109], v[102:103]
	v_cvt_f32_f16_sdwa v109, v97 dst_sel:DWORD dst_unused:UNUSED_PAD src0_sel:WORD_1
	v_cvt_f32_f16_e32 v108, v97
	v_cvt_f32_f16_sdwa v97, v96 dst_sel:DWORD dst_unused:UNUSED_PAD src0_sel:WORD_1
	v_cvt_f32_f16_e32 v96, v96
	v_pk_add_f32 v[98:99], v[110:111], v[98:99]
	v_pk_add_f32 v[104:105], v[104:105], v[108:109]
	v_mov_b32_e32 v108, v103
	v_mov_b32_e32 v109, v105
	v_pk_add_f32 v[96:97], v[106:107], v[96:97]
	v_mov_b32_e32 v106, v102
	v_mov_b32_e32 v107, v104
	v_pk_mul_f32 v[108:109], v[108:109], v[108:109]
	v_pk_fma_f32 v[100:101], v[112:113], v[112:113], v[100:101]
	v_pk_fma_f32 v[106:107], v[106:107], v[106:107], v[108:109]
	v_mov_b32_e32 v108, v98
	v_mov_b32_e32 v109, v96
	v_mov_b32_e32 v110, v99
	v_mov_b32_e32 v111, v97
	v_pk_fma_f32 v[106:107], v[108:109], v[108:109], v[106:107]
	v_add_f32_e32 v95, v100, v101
	v_pk_fma_f32 v[106:107], v[110:111], v[110:111], v[106:107]
	v_lshl_add_u64 v[34:35], v[34:35], 0, s[12:13]
	v_add_f32_e32 v95, v95, v106
	v_add_f32_e32 v95, v95, v107
	v_mov_b32_e32 v100, v95
	s_nop 1
	v_permlane32_swap_b32 v100, v95
	s_waitcnt lgkmcnt(0)
	v_add_f32_e32 v95, v95, v100
	v_mov_b32_e32 v100, v95
	s_nop 1
	v_permlane16_swap_b32 v100, v95
	s_waitcnt lgkmcnt(0)
	v_add_f32_e32 v95, v95, v100
	s_nop 1
	v_mov_b32_dpp v100, v95 row_ror:8 row_mask:0xf bank_mask:0xf
	s_waitcnt lgkmcnt(0)
	v_add_f32_e32 v95, v95, v100
	s_nop 1
	v_mov_b32_dpp v100, v95 row_half_mirror row_mask:0xf bank_mask:0xf
	s_nop 1
	v_mov_b32_dpp v100, v100 quad_perm:[3,2,1,0] row_mask:0xf bank_mask:0xf
	s_waitcnt lgkmcnt(0)
	v_add_f32_e32 v95, v95, v100
	s_nop 1
	v_mov_b32_dpp v100, v95 quad_perm:[2,3,0,1] row_mask:0xf bank_mask:0xf
	s_waitcnt lgkmcnt(0)
	v_add_f32_e32 v95, v95, v100
	s_nop 1
	v_mov_b32_dpp v100, v95 quad_perm:[1,0,3,2] row_mask:0xf bank_mask:0xf
	s_waitcnt lgkmcnt(0)
	v_add_f32_e32 v95, v95, v100
	v_fmamk_f32 v95, v95, 0x3a800000, v191
	v_cmp_gt_f32_e32 vcc, s18, v95
	v_mul_f32_e32 v100, 0x4b800000, v95
	s_nop 0
	v_cndmask_b32_e32 v95, v95, v100, vcc
	v_rsq_f32_e32 v95, v95
	s_nop 0
	v_mul_f32_e32 v100, 0x45800000, v95
	v_cndmask_b32_e32 v100, v95, v100, vcc
	v_pk_mul_f32 v[84:85], v[84:85], v[100:101] op_sel_hi:[1,0]
	v_pk_mul_f32 v[0:1], v[124:125], v[84:85]
	v_pk_mul_f32 v[84:85], v[90:91], v[100:101] op_sel_hi:[1,0]
	s_nop 0
	v_pk_mul_f32 v[2:3], v[126:127], v[84:85]
	global_store_dwordx4 v[72:73], v[0:3], off
	s_nop 1
	v_pk_mul_f32 v[84:85], v[86:87], v[100:101] op_sel_hi:[1,0]
	v_pk_mul_f32 v[0:1], v[128:129], v[84:85]
	v_pk_mul_f32 v[84:85], v[88:89], v[100:101] op_sel_hi:[1,0]
	s_nop 0
	v_pk_mul_f32 v[2:3], v[130:131], v[84:85]
	global_store_dwordx4 v[72:73], v[0:3], off offset:16
	s_nop 1
	v_pk_mul_f32 v[84:85], v[102:103], v[100:101] op_sel_hi:[1,0]
	v_pk_mul_f32 v[0:1], v[84:85], v[132:133]
	v_pk_mul_f32 v[84:85], v[98:99], v[100:101] op_sel_hi:[1,0]
	s_nop 0
	v_pk_mul_f32 v[2:3], v[84:85], v[134:135]
	global_store_dwordx4 v[72:73], v[0:3], off offset:32
	s_nop 1
	v_pk_mul_f32 v[84:85], v[104:105], v[100:101] op_sel_hi:[1,0]
	v_pk_mul_f32 v[0:1], v[84:85], v[136:137]
	v_pk_mul_f32 v[84:85], v[96:97], v[100:101] op_sel_hi:[1,0]
	s_nop 0
	v_pk_mul_f32 v[2:3], v[84:85], v[138:139]
	global_store_dwordx4 v[72:73], v[0:3], off offset:48
	s_nop 1
	v_mov_b32_e32 v0, v94
	s_andn2_b64 exec, exec, s[10:11]
	s_cbranch_execnz .LBB0_762

.LBB0_770:
	s_cmpk_ge_i32 s56, 0x70
	s_cselect_b64 s[10:11], -1, 0
	ds_bpermute_b32 v6, v97, v96
	s_and_b64 vcc, s[10:11], s[48:49]
	v_cndmask_b32_e32 v94, v0, v98, vcc
	v_ashrrev_i32_e32 v95, 31, v94
	s_add_i32 s10, s56, 16
	s_and_b32 s10, s10, 0x70
	v_lshlrev_b64 v[94:95], 9, v[94:95]
	v_lshl_add_u64 v[94:95], s[94:95], 0, v[94:95]
	s_lshl_b32 s36, s10, 2
	s_waitcnt lgkmcnt(0)
	s_waitcnt vmcnt(32)
	v_mov_b32_e32 v96, v122
	v_ashrrev_i32_e32 v7, 31, v6
	v_lshl_add_u64 v[94:95], v[94:95], 0, s[36:37]
	v_lshl_add_u64 v[6:7], v[6:7], 3, s[88:89]
	v_lshl_add_u64 v[94:95], v[94:95], 0, v[144:145]
	global_load_dwordx2 v[6:7], v[6:7], off
	s_nop 0
	global_load_dword v8, v[4:5], off
	global_load_dword v122, v[94:95], off
	s_waitcnt vmcnt(19)
	v_dot8_i32_i4 v9, v20, v1, 0
	v_dot8_i32_i4 v94, v20, v10, 0
	v_dot8_i32_i4 v9, v21, v11, v9
	v_dot8_i32_i4 v94, v21, v12, v94
	v_dot8_i32_i4 v20, v22, v1, 0
	v_dot8_i32_i4 v21, v22, v10, 0
	v_dot8_i32_i4 v20, v23, v11, v20
	v_dot8_i32_i4 v21, v23, v12, v21
	v_lshl_add_u32 v9, v9, 4, v94
	s_add_i32 s56, s56, 16
	s_nop 0
	v_lshl_add_u32 v94, v20, 4, v21
	s_waitcnt vmcnt(19)
	v_dot8_i32_i4 v20, v24, v1, 0
	v_dot8_i32_i4 v21, v24, v10, 0
	v_dot8_i32_i4 v20, v25, v11, v20
	v_dot8_i32_i4 v21, v25, v12, v21
	v_lshl_add_u64 v[4:5], v[4:5], 0, 64
	s_nop 1
	v_lshl_add_u32 v95, v20, 4, v21
	v_dot8_i32_i4 v20, v26, v1, 0
	v_dot8_i32_i4 v21, v26, v10, 0
	v_dot8_i32_i4 v20, v27, v11, v20
	v_dot8_i32_i4 v21, v27, v12, v21
	v_readlane_b32 s10, v96, 0
	s_ashr_i32 s11, s10, 31
	v_readlane_b32 s12, v96, 1
	v_lshl_add_u32 v106, v20, 4, v21
	v_dot8_i32_i4 v20, v28, v1, 0
	v_dot8_i32_i4 v21, v28, v10, 0
	v_dot8_i32_i4 v20, v29, v11, v20
	v_dot8_i32_i4 v21, v29, v12, v21
	s_lshl_b64 s[10:11], s[10:11], 9
	s_ashr_i32 s13, s12, 31
	v_readlane_b32 s14, v96, 2
	v_lshl_add_u32 v107, v20, 4, v21
	v_dot8_i32_i4 v20, v30, v1, 0
	v_dot8_i32_i4 v21, v30, v10, 0
	v_dot8_i32_i4 v20, v31, v11, v20
	v_dot8_i32_i4 v21, v31, v12, v21
	s_lshl_b64 s[12:13], s[12:13], 9
	s_ashr_i32 s15, s14, 31
	v_readlane_b32 s16, v96, 3
	v_lshl_add_u32 v108, v20, 4, v21
	v_dot8_i32_i4 v20, v32, v1, 0
	v_dot8_i32_i4 v21, v32, v10, 0
	v_dot8_i32_i4 v20, v33, v11, v20
	v_dot8_i32_i4 v21, v33, v12, v21
	s_lshl_b64 s[14:15], s[14:15], 9
	s_ashr_i32 s17, s16, 31
	s_nop 0
	v_lshl_add_u32 v109, v20, 4, v21
	v_dot8_i32_i4 v20, v34, v1, 0
	v_dot8_i32_i4 v21, v34, v10, 0
	v_dot8_i32_i4 v20, v35, v11, v20
	v_dot8_i32_i4 v21, v35, v12, v21
	v_readlane_b32 s18, v96, 4
	s_add_u32 s66, s12, s62
	s_addc_u32 s67, s13, s63
	global_load_dwordx2 v[22:23], v121, s[66:67]
	v_lshl_add_u32 v110, v20, 4, v21
	v_dot8_i32_i4 v20, v36, v1, 0
	v_dot8_i32_i4 v21, v36, v10, 0
	v_dot8_i32_i4 v20, v37, v11, v20
	v_dot8_i32_i4 v21, v37, v12, v21
	s_lshl_b64 s[16:17], s[16:17], 9
	s_ashr_i32 s19, s18, 31
	v_readlane_b32 s20, v96, 5
	v_lshl_add_u32 v111, v20, 4, v21
	v_dot8_i32_i4 v20, v38, v1, 0
	v_dot8_i32_i4 v21, v38, v10, 0
	v_dot8_i32_i4 v20, v39, v11, v20
	v_dot8_i32_i4 v21, v39, v12, v21
	s_setprio 2
	v_permlane32_swap_b32 v9, v111
	s_nop 1
	v_lshl_add_u32 v112, v20, 4, v21
	v_dot8_i32_i4 v20, v40, v1, 0
	v_dot8_i32_i4 v21, v40, v10, 0
	v_dot8_i32_i4 v20, v41, v11, v20
	v_dot8_i32_i4 v21, v41, v12, v21
	s_waitcnt lgkmcnt(0)
	v_add_u32_e32 v9, v9, v111
	v_permlane32_swap_b32 v94, v112
	v_lshl_add_u32 v113, v20, 4, v21
	v_dot8_i32_i4 v20, v60, v1, 0
	v_dot8_i32_i4 v21, v60, v10, 0
	v_dot8_i32_i4 v20, v61, v11, v20
	v_dot8_i32_i4 v21, v61, v12, v21
	s_waitcnt lgkmcnt(0)
	v_add_u32_e32 v94, v94, v112
	v_permlane32_swap_b32 v95, v113
	v_lshl_add_u32 v114, v20, 4, v21
	v_dot8_i32_i4 v20, v58, v1, 0
	v_dot8_i32_i4 v21, v58, v10, 0
	v_dot8_i32_i4 v20, v59, v11, v20
	v_dot8_i32_i4 v21, v59, v12, v21
	s_waitcnt lgkmcnt(0)
	v_add_u32_e32 v95, v95, v113
	v_permlane32_swap_b32 v106, v114
	v_lshl_add_u32 v115, v20, 4, v21
	v_dot8_i32_i4 v20, v56, v1, 0
	v_dot8_i32_i4 v21, v56, v10, 0
	v_dot8_i32_i4 v20, v57, v11, v20
	v_dot8_i32_i4 v21, v57, v12, v21
	s_waitcnt lgkmcnt(0)
	v_add_u32_e32 v106, v106, v114
	v_permlane32_swap_b32 v107, v115
	v_lshl_add_u32 v116, v20, 4, v21
	v_dot8_i32_i4 v20, v54, v1, 0
	v_dot8_i32_i4 v21, v54, v10, 0
	v_dot8_i32_i4 v20, v55, v11, v20
	v_dot8_i32_i4 v21, v55, v12, v21
	s_waitcnt lgkmcnt(0)
	v_add_u32_e32 v107, v107, v115
	v_permlane32_swap_b32 v108, v116
	v_lshl_add_u32 v117, v20, 4, v21
	v_dot8_i32_i4 v20, v52, v1, 0
	v_dot8_i32_i4 v21, v52, v10, 0
	v_dot8_i32_i4 v20, v53, v11, v20
	v_dot8_i32_i4 v21, v53, v12, v21
	s_waitcnt lgkmcnt(0)
	v_add_u32_e32 v108, v108, v116
	v_permlane32_swap_b32 v109, v117
	v_lshl_add_u32 v118, v20, 4, v21
	s_waitcnt lgkmcnt(0)
	v_add_u32_e32 v109, v109, v117
	v_permlane32_swap_b32 v110, v118
	s_add_u32 s66, s10, s62
	s_addc_u32 s67, s11, s63
	global_load_dwordx2 v[20:21], v121, s[66:67]
	s_add_u32 s66, s14, s62
	s_addc_u32 s67, s15, s63
	global_load_dwordx2 v[24:25], v121, s[66:67]
	s_waitcnt lgkmcnt(0)
	v_add_u32_e32 v110, v110, v118
	v_permlane16_swap_b32 v9, v107
	s_lshl_b64 s[18:19], s[18:19], 9
	s_ashr_i32 s21, s20, 31
	v_readlane_b32 s22, v96, 6
	s_add_u32 s66, s16, s62
	s_addc_u32 s67, s17, s63
	global_load_dwordx2 v[26:27], v121, s[66:67]
	s_waitcnt lgkmcnt(0)
	v_add_u32_e32 v9, v9, v107
	v_permlane16_swap_b32 v94, v108
	s_lshl_b64 s[20:21], s[20:21], 9
	s_ashr_i32 s23, s22, 31
	s_waitcnt lgkmcnt(0)
	v_add_u32_e32 v94, v94, v108
	v_permlane16_swap_b32 v95, v109
	v_readlane_b32 s24, v96, 7
	s_add_u32 s66, s18, s62
	s_addc_u32 s67, s19, s63
	global_load_dwordx2 v[28:29], v121, s[66:67]
	s_waitcnt lgkmcnt(0)
	v_add_u32_e32 v95, v95, v109
	v_permlane16_swap_b32 v106, v110
	s_lshl_b64 s[22:23], s[22:23], 9
	s_ashr_i32 s25, s24, 31
	v_readlane_b32 s26, v96, 8
	s_waitcnt lgkmcnt(0)
	v_add_u32_e32 v106, v106, v110
	v_cndmask_b32_e64 v107, v9, v95, s[44:45]
	v_cndmask_b32_e64 v9, v95, v9, s[44:45]
	s_nop 0
	s_add_u32 s66, s20, s62
	s_addc_u32 s67, s21, s63
	global_load_dwordx2 v[30:31], v121, s[66:67]
	s_lshl_b64 s[24:25], s[24:25], 9
	s_ashr_i32 s27, s26, 31
	s_waitcnt lgkmcnt(0)
	v_add_u32_dpp v9, v107, v9 row_ror:8 row_mask:0xf bank_mask:0xf
	v_cndmask_b32_e64 v95, v94, v106, s[44:45]
	s_nop 1
	v_cndmask_b32_e64 v94, v106, v94, s[44:45]
	v_readlane_b32 s28, v96, 9
	s_add_u32 s66, s22, s62
	s_addc_u32 s67, s23, s63
	global_load_dwordx2 v[32:33], v121, s[66:67]
	s_waitcnt lgkmcnt(0)
	v_add_u32_dpp v94, v95, v94 row_ror:8 row_mask:0xf bank_mask:0xf
	v_cndmask_b32_e64 v95, v9, v94, s[46:47]
	v_cndmask_b32_e64 v9, v94, v9, s[46:47]
	s_nop 0
	v_mov_b32_dpp v94, v95 row_half_mirror row_mask:0xf bank_mask:0xf
	s_nop 1
	s_lshl_b64 s[26:27], s[26:27], 9
	s_ashr_i32 s29, s28, 31
	v_readlane_b32 s30, v96, 10
	s_add_u32 s66, s24, s62
	s_addc_u32 s67, s25, s63
	global_load_dwordx2 v[34:35], v121, s[66:67]
	s_waitcnt lgkmcnt(0)
	v_add_u32_dpp v9, v94, v9 quad_perm:[3,2,1,0] row_mask:0xf bank_mask:0xf
	s_nop 1
	s_lshl_b64 s[28:29], s[28:29], 9
	s_ashr_i32 s31, s30, 31
	v_readlane_b32 s34, v96, 11
	s_waitcnt lgkmcnt(0)
	v_add_u32_dpp v9, v9, v9 quad_perm:[2,3,0,1] row_mask:0xf bank_mask:0xf
	s_nop 1
	s_add_u32 s66, s26, s62
	s_addc_u32 s67, s27, s63
	global_load_dwordx2 v[36:37], v121, s[66:67]
	s_lshl_b64 s[30:31], s[30:31], 9
	s_ashr_i32 s35, s34, 31
	s_waitcnt lgkmcnt(0)
	v_add_u32_dpp v9, v9, v9 quad_perm:[1,0,3,2] row_mask:0xf bank_mask:0xf
	s_waitcnt vmcnt(10)
	v_mul_f32_e32 v7, v13, v7
	v_cvt_f32_i32_e32 v9, v9
	v_add_f32_e32 v9, v14, v9
	v_mul_f32_e32 v7, v7, v9
	v_mul_f32_e32 v9, 0x3d372713, v7
	v_mul_f32_e32 v9, v7, v9
	v_fma_f32 v9, v7, v9, v7
	v_mul_f32_e32 v9, 0x3fcc422a, v9
	v_mul_f32_e32 v9, 0xbfb8aa3b, v9
	v_exp_f32_e32 v9, v9
	v_readlane_b32 s38, v96, 12
	s_add_u32 s66, s28, s62
	s_addc_u32 s67, s29, s63
	global_load_dwordx2 v[38:39], v121, s[66:67]
	v_add_f32_e32 v9, 1.0, v9
	v_rcp_f32_e32 v9, v9
	s_lshl_b64 s[34:35], s[34:35], 9
	s_ashr_i32 s39, s38, 31
	v_pk_mul_f32 v[6:7], v[6:7], v[8:9]
	s_waitcnt vmcnt(28)
	v_alignbit_b32 v224, v92, v92, 4
	v_pk_mul_f32 v[6:7], v[6:7], v[6:7] op_sel:[0,1] op_sel_hi:[1,0]
	v_cvt_f16_f32_e32 v120, v6
	s_setprio 0
	s_lshl_b64 s[38:39], s[38:39], 9
	v_readlane_b32 s50, v96, 13
	v_readlane_b32 s52, v96, 14
	v_readlane_b32 s54, v96, 15
	s_ashr_i32 s51, s50, 31
	s_ashr_i32 s53, s52, 31
	s_ashr_i32 s55, s54, 31
	s_lshl_b64 s[50:51], s[50:51], 9
	s_lshl_b64 s[52:53], s[52:53], 9
	s_lshl_b64 s[54:55], s[54:55], 9
	s_add_u32 s66, s30, s62
	s_addc_u32 s67, s31, s63
	global_load_dwordx2 v[40:41], v121, s[66:67]
	s_add_u32 s66, s34, s62
	s_addc_u32 s67, s35, s63
	global_load_dwordx2 v[60:61], v121, s[66:67]
	s_add_u32 s66, s38, s62
	s_addc_u32 s67, s39, s63
	global_load_dwordx2 v[58:59], v121, s[66:67]
	s_add_u32 s66, s50, s62
	s_addc_u32 s67, s51, s63
	global_load_dwordx2 v[56:57], v121, s[66:67]
	s_add_u32 s66, s52, s62
	s_addc_u32 s67, s53, s63
	global_load_dwordx2 v[54:55], v121, s[66:67]
	s_add_u32 s66, s54, s62
	s_addc_u32 s67, s55, s63
	global_load_dwordx2 v[52:53], v121, s[66:67]
	v_and_b32_e32 v8, 0x7070707, v92
	v_readlane_b32 s36, v120, 0
	v_and_b32_e32 v9, 0x7070707, v224
	v_perm_b32 v8, s2, v205, v8
	v_perm_b32 v9, s2, v205, v9
	v_and_or_b32 v8, v92, s4, v8
	v_and_or_b32 v9, v224, s4, v9
	v_perm_b32 v92, v9, v8, s5
	v_perm_b32 v94, v9, v8, s33
	v_perm_b32 v95, v9, v8, s0
	v_perm_b32 v8, v9, v8, s1
	v_pk_fma_f16 v8, v8, s36, v102 op_sel_hi:[1,0,1]
	v_alignbit_b32 v225, v93, v93, 4
	v_pk_fma_f16 v9, v92, s36, v105 op_sel_hi:[1,0,1]
	v_pk_fma_f16 v92, v94, s36, v104 op_sel_hi:[1,0,1]
	v_pk_fma_f16 v94, v95, s36, v103 op_sel_hi:[1,0,1]
	v_and_b32_e32 v95, 0x7070707, v93
	v_and_b32_e32 v102, 0x7070707, v225
	v_perm_b32 v95, s2, v205, v95
	v_perm_b32 v102, s2, v205, v102
	v_and_or_b32 v95, v93, s4, v95
	v_and_or_b32 v93, v225, s4, v102
	v_perm_b32 v102, v93, v95, s5
	v_perm_b32 v103, v93, v95, s33
	v_perm_b32 v104, v93, v95, s0
	v_perm_b32 v93, v93, v95, s1
	v_pk_fma_f16 v95, v102, s36, v101 op_sel_hi:[1,0,1]
	v_readlane_b32 s59, v120, 4
	s_waitcnt vmcnt(33)
	v_alignbit_b32 v224, v90, v90, 4
	v_pk_fma_f16 v100, v103, s36, v100 op_sel_hi:[1,0,1]
	v_pk_fma_f16 v99, v104, s36, v99 op_sel_hi:[1,0,1]
	v_pk_fma_f16 v7, v93, s36, v15 op_sel_hi:[1,0,1]
	v_and_b32_e32 v93, 0x7070707, v90
	v_and_b32_e32 v101, 0x7070707, v224
	v_perm_b32 v93, s2, v205, v93
	v_perm_b32 v101, s2, v205, v101
	v_and_or_b32 v93, v90, s4, v93
	v_and_or_b32 v90, v224, s4, v101
	v_perm_b32 v103, v90, v93, s0
	v_perm_b32 v101, v90, v93, s5
	v_perm_b32 v102, v90, v93, s33
	v_perm_b32 v90, v90, v93, s1
	v_pk_fma_f16 v93, v103, s59, v94 op_sel_hi:[1,0,1]
	v_alignbit_b32 v225, v91, v91, 4
	v_pk_fma_f16 v8, v90, s59, v8 op_sel_hi:[1,0,1]
	v_and_b32_e32 v90, 0x7070707, v91
	v_and_b32_e32 v94, 0x7070707, v225
	v_pk_fma_f16 v9, v101, s59, v9 op_sel_hi:[1,0,1]
	v_perm_b32 v90, s2, v205, v90
	v_perm_b32 v94, s2, v205, v94
	v_and_or_b32 v90, v91, s4, v90
	v_and_or_b32 v91, v225, s4, v94
	v_pk_fma_f16 v92, v102, s59, v92 op_sel_hi:[1,0,1]
	v_perm_b32 v94, v91, v90, s5
	v_perm_b32 v102, v91, v90, s0
	v_perm_b32 v101, v91, v90, s33
	v_perm_b32 v90, v91, v90, s1
	v_pk_fma_f16 v91, v94, s59, v95 op_sel_hi:[1,0,1]
	v_pk_fma_f16 v95, v102, s59, v99 op_sel_hi:[1,0,1]
	v_readlane_b32 s60, v120, 8
	s_waitcnt vmcnt(32)
	v_alignbit_b32 v224, v88, v88, 4
	v_pk_fma_f16 v94, v101, s59, v100 op_sel_hi:[1,0,1]
	v_pk_fma_f16 v7, v90, s59, v7 op_sel_hi:[1,0,1]
	v_and_b32_e32 v90, 0x7070707, v88
	v_and_b32_e32 v99, 0x7070707, v224
	v_perm_b32 v90, s2, v205, v90
	v_perm_b32 v99, s2, v205, v99
	v_and_or_b32 v90, v88, s4, v90
	v_and_or_b32 v88, v224, s4, v99
	v_perm_b32 v100, v88, v90, s33
	v_perm_b32 v101, v88, v90, s0
	v_perm_b32 v99, v88, v90, s5
	v_perm_b32 v88, v88, v90, s1
	v_pk_fma_f16 v90, v100, s60, v92 op_sel_hi:[1,0,1]
	v_pk_fma_f16 v92, v101, s60, v93 op_sel_hi:[1,0,1]
	v_alignbit_b32 v225, v89, v89, 4
	v_pk_fma_f16 v8, v88, s60, v8 op_sel_hi:[1,0,1]
	v_and_b32_e32 v88, 0x7070707, v89
	v_and_b32_e32 v93, 0x7070707, v225
	v_pk_fma_f16 v9, v99, s60, v9 op_sel_hi:[1,0,1]
	v_perm_b32 v88, s2, v205, v88
	v_perm_b32 v93, s2, v205, v93
	v_and_or_b32 v88, v89, s4, v88
	v_and_or_b32 v89, v225, s4, v93
	v_perm_b32 v93, v89, v88, s5
	v_perm_b32 v99, v89, v88, s33
	v_perm_b32 v100, v89, v88, s0
	v_perm_b32 v88, v89, v88, s1
	v_pk_fma_f16 v89, v93, s60, v91 op_sel_hi:[1,0,1]
	v_pk_fma_f16 v91, v99, s60, v94 op_sel_hi:[1,0,1]
	v_readlane_b32 s36, v120, 12
	s_waitcnt vmcnt(31)
	v_alignbit_b32 v224, v86, v86, 4
	v_pk_fma_f16 v93, v100, s60, v95 op_sel_hi:[1,0,1]
	v_pk_fma_f16 v7, v88, s60, v7 op_sel_hi:[1,0,1]
	v_and_b32_e32 v88, 0x7070707, v86
	v_and_b32_e32 v94, 0x7070707, v224
	v_perm_b32 v88, s2, v205, v88
	v_perm_b32 v94, s2, v205, v94
	v_and_or_b32 v88, v86, s4, v88
	v_and_or_b32 v86, v224, s4, v94
	v_perm_b32 v95, v86, v88, s33
	v_perm_b32 v99, v86, v88, s0
	v_perm_b32 v94, v86, v88, s5
	v_perm_b32 v86, v86, v88, s1
	v_pk_fma_f16 v88, v95, s36, v90 op_sel_hi:[1,0,1]
	v_pk_fma_f16 v90, v99, s36, v92 op_sel_hi:[1,0,1]
	v_alignbit_b32 v225, v87, v87, 4
	v_pk_fma_f16 v8, v86, s36, v8 op_sel_hi:[1,0,1]
	v_and_b32_e32 v86, 0x7070707, v87
	v_and_b32_e32 v92, 0x7070707, v225
	v_pk_fma_f16 v9, v94, s36, v9 op_sel_hi:[1,0,1]
	v_perm_b32 v86, s2, v205, v86
	v_perm_b32 v92, s2, v205, v92
	v_and_or_b32 v86, v87, s4, v86
	v_and_or_b32 v87, v225, s4, v92
	v_perm_b32 v92, v87, v86, s5
	v_perm_b32 v94, v87, v86, s33
	v_perm_b32 v95, v87, v86, s0
	v_perm_b32 v86, v87, v86, s1
	v_pk_fma_f16 v87, v92, s36, v89 op_sel_hi:[1,0,1]
	v_readlane_b32 s59, v120, 16
	s_waitcnt vmcnt(30)
	v_alignbit_b32 v224, v84, v84, 4
	v_pk_fma_f16 v89, v94, s36, v91 op_sel_hi:[1,0,1]
	v_pk_fma_f16 v91, v95, s36, v93 op_sel_hi:[1,0,1]
	v_pk_fma_f16 v7, v86, s36, v7 op_sel_hi:[1,0,1]
	v_and_b32_e32 v86, 0x7070707, v84
	v_and_b32_e32 v92, 0x7070707, v224
	v_perm_b32 v86, s2, v205, v86
	v_perm_b32 v92, s2, v205, v92
	v_and_or_b32 v86, v84, s4, v86
	v_and_or_b32 v84, v224, s4, v92
	v_perm_b32 v93, v84, v86, s33
	v_perm_b32 v94, v84, v86, s0
	v_perm_b32 v92, v84, v86, s5
	v_perm_b32 v84, v84, v86, s1
	v_pk_fma_f16 v86, v93, s59, v88 op_sel_hi:[1,0,1]
	v_pk_fma_f16 v88, v94, s59, v90 op_sel_hi:[1,0,1]
	v_alignbit_b32 v225, v85, v85, 4
	v_pk_fma_f16 v8, v84, s59, v8 op_sel_hi:[1,0,1]
	v_and_b32_e32 v84, 0x7070707, v85
	v_and_b32_e32 v90, 0x7070707, v225
	v_pk_fma_f16 v9, v92, s59, v9 op_sel_hi:[1,0,1]
	v_perm_b32 v84, s2, v205, v84
	v_perm_b32 v90, s2, v205, v90
	v_and_or_b32 v84, v85, s4, v84
	v_and_or_b32 v85, v225, s4, v90
	v_perm_b32 v90, v85, v84, s5
	v_perm_b32 v92, v85, v84, s33
	v_perm_b32 v93, v85, v84, s0
	v_perm_b32 v84, v85, v84, s1
	v_pk_fma_f16 v85, v90, s59, v87 op_sel_hi:[1,0,1]
	v_readlane_b32 s60, v120, 20
	s_waitcnt vmcnt(29)
	v_alignbit_b32 v224, v82, v82, 4
	v_pk_fma_f16 v87, v92, s59, v89 op_sel_hi:[1,0,1]
	v_pk_fma_f16 v89, v93, s59, v91 op_sel_hi:[1,0,1]
	v_pk_fma_f16 v7, v84, s59, v7 op_sel_hi:[1,0,1]
	v_and_b32_e32 v84, 0x7070707, v82
	v_and_b32_e32 v90, 0x7070707, v224
	v_perm_b32 v84, s2, v205, v84
	v_perm_b32 v90, s2, v205, v90
	v_and_or_b32 v84, v82, s4, v84
	v_and_or_b32 v82, v224, s4, v90
	v_perm_b32 v91, v82, v84, s33
	v_perm_b32 v92, v82, v84, s0
	v_perm_b32 v90, v82, v84, s5
	v_perm_b32 v82, v82, v84, s1
	v_pk_fma_f16 v84, v91, s60, v86 op_sel_hi:[1,0,1]
	v_pk_fma_f16 v86, v92, s60, v88 op_sel_hi:[1,0,1]
	s_add_u32 s66, s10, s64
	s_addc_u32 s67, s11, s65
	global_load_dwordx2 v[92:93], v121, s[66:67]
	v_alignbit_b32 v225, v83, v83, 4
	v_pk_fma_f16 v8, v82, s60, v8 op_sel_hi:[1,0,1]
	v_and_b32_e32 v82, 0x7070707, v83
	v_and_b32_e32 v88, 0x7070707, v225
	v_pk_fma_f16 v9, v90, s60, v9 op_sel_hi:[1,0,1]
	v_perm_b32 v82, s2, v205, v82
	v_perm_b32 v88, s2, v205, v88
	v_and_or_b32 v82, v83, s4, v82
	v_and_or_b32 v83, v225, s4, v88
	v_perm_b32 v88, v83, v82, s5
	v_perm_b32 v90, v83, v82, s33
	v_perm_b32 v91, v83, v82, s0
	v_perm_b32 v82, v83, v82, s1
	v_pk_fma_f16 v83, v88, s60, v85 op_sel_hi:[1,0,1]
	v_readlane_b32 s36, v120, 24
	s_waitcnt vmcnt(29)
	v_alignbit_b32 v224, v80, v80, 4
	v_pk_fma_f16 v85, v90, s60, v87 op_sel_hi:[1,0,1]
	v_pk_fma_f16 v87, v91, s60, v89 op_sel_hi:[1,0,1]
	v_pk_fma_f16 v7, v82, s60, v7 op_sel_hi:[1,0,1]
	v_and_b32_e32 v82, 0x7070707, v80
	v_and_b32_e32 v88, 0x7070707, v224
	v_perm_b32 v82, s2, v205, v82
	v_perm_b32 v88, s2, v205, v88
	v_and_or_b32 v82, v80, s4, v82
	v_and_or_b32 v80, v224, s4, v88
	v_perm_b32 v89, v80, v82, s33
	v_perm_b32 v90, v80, v82, s0
	v_perm_b32 v88, v80, v82, s5
	v_perm_b32 v80, v80, v82, s1
	v_pk_fma_f16 v82, v89, s36, v84 op_sel_hi:[1,0,1]
	v_pk_fma_f16 v84, v90, s36, v86 op_sel_hi:[1,0,1]
	s_add_u32 s66, s12, s64
	s_addc_u32 s67, s13, s65
	global_load_dwordx2 v[90:91], v121, s[66:67]
	v_alignbit_b32 v225, v81, v81, 4
	v_pk_fma_f16 v8, v80, s36, v8 op_sel_hi:[1,0,1]
	v_and_b32_e32 v80, 0x7070707, v81
	v_and_b32_e32 v86, 0x7070707, v225
	v_pk_fma_f16 v9, v88, s36, v9 op_sel_hi:[1,0,1]
	v_perm_b32 v80, s2, v205, v80
	v_perm_b32 v86, s2, v205, v86
	v_and_or_b32 v80, v81, s4, v80
	v_and_or_b32 v81, v225, s4, v86
	v_perm_b32 v86, v81, v80, s5
	v_perm_b32 v88, v81, v80, s33
	v_perm_b32 v89, v81, v80, s0
	v_perm_b32 v80, v81, v80, s1
	v_pk_fma_f16 v81, v86, s36, v83 op_sel_hi:[1,0,1]
	v_readlane_b32 s59, v120, 28
	s_waitcnt vmcnt(29)
	v_alignbit_b32 v224, v78, v78, 4
	v_pk_fma_f16 v83, v88, s36, v85 op_sel_hi:[1,0,1]
	v_pk_fma_f16 v85, v89, s36, v87 op_sel_hi:[1,0,1]
	v_pk_fma_f16 v7, v80, s36, v7 op_sel_hi:[1,0,1]
	v_and_b32_e32 v80, 0x7070707, v78
	v_and_b32_e32 v86, 0x7070707, v224
	v_perm_b32 v80, s2, v205, v80
	v_perm_b32 v86, s2, v205, v86
	v_and_or_b32 v80, v78, s4, v80
	v_and_or_b32 v78, v224, s4, v86
	v_perm_b32 v87, v78, v80, s33
	v_perm_b32 v88, v78, v80, s0
	v_perm_b32 v86, v78, v80, s5
	v_perm_b32 v78, v78, v80, s1
	v_pk_fma_f16 v80, v87, s59, v82 op_sel_hi:[1,0,1]
	v_pk_fma_f16 v82, v88, s59, v84 op_sel_hi:[1,0,1]
	s_add_u32 s66, s14, s64
	s_addc_u32 s67, s15, s65
	global_load_dwordx2 v[88:89], v121, s[66:67]
	v_alignbit_b32 v225, v79, v79, 4
	v_pk_fma_f16 v8, v78, s59, v8 op_sel_hi:[1,0,1]
	v_and_b32_e32 v78, 0x7070707, v79
	v_and_b32_e32 v84, 0x7070707, v225
	v_pk_fma_f16 v9, v86, s59, v9 op_sel_hi:[1,0,1]
	v_perm_b32 v78, s2, v205, v78
	v_perm_b32 v84, s2, v205, v84
	v_and_or_b32 v78, v79, s4, v78
	v_and_or_b32 v79, v225, s4, v84
	v_perm_b32 v84, v79, v78, s5
	v_perm_b32 v86, v79, v78, s33
	v_perm_b32 v87, v79, v78, s0
	v_perm_b32 v78, v79, v78, s1
	v_pk_fma_f16 v79, v84, s59, v81 op_sel_hi:[1,0,1]
	v_readlane_b32 s60, v120, 32
	s_waitcnt vmcnt(29)
	v_alignbit_b32 v224, v76, v76, 4
	v_pk_fma_f16 v81, v86, s59, v83 op_sel_hi:[1,0,1]
	v_pk_fma_f16 v83, v87, s59, v85 op_sel_hi:[1,0,1]
	v_pk_fma_f16 v7, v78, s59, v7 op_sel_hi:[1,0,1]
	v_and_b32_e32 v78, 0x7070707, v76
	v_and_b32_e32 v84, 0x7070707, v224
	v_perm_b32 v78, s2, v205, v78
	v_perm_b32 v84, s2, v205, v84
	v_and_or_b32 v78, v76, s4, v78
	v_and_or_b32 v76, v224, s4, v84
	v_perm_b32 v85, v76, v78, s33
	v_perm_b32 v86, v76, v78, s0
	v_perm_b32 v84, v76, v78, s5
	v_perm_b32 v76, v76, v78, s1
	v_pk_fma_f16 v78, v85, s60, v80 op_sel_hi:[1,0,1]
	v_pk_fma_f16 v80, v86, s60, v82 op_sel_hi:[1,0,1]
	s_add_u32 s66, s16, s64
	s_addc_u32 s67, s17, s65
	global_load_dwordx2 v[86:87], v121, s[66:67]
	v_alignbit_b32 v225, v77, v77, 4
	v_pk_fma_f16 v8, v76, s60, v8 op_sel_hi:[1,0,1]
	v_and_b32_e32 v76, 0x7070707, v77
	v_and_b32_e32 v82, 0x7070707, v225
	v_pk_fma_f16 v9, v84, s60, v9 op_sel_hi:[1,0,1]
	v_perm_b32 v76, s2, v205, v76
	v_perm_b32 v82, s2, v205, v82
	v_and_or_b32 v76, v77, s4, v76
	v_and_or_b32 v77, v225, s4, v82
	v_perm_b32 v82, v77, v76, s5
	v_perm_b32 v84, v77, v76, s33
	v_perm_b32 v85, v77, v76, s0
	v_perm_b32 v76, v77, v76, s1
	v_pk_fma_f16 v77, v82, s60, v79 op_sel_hi:[1,0,1]
	v_readlane_b32 s36, v120, 36
	s_waitcnt vmcnt(28)
	v_alignbit_b32 v224, v70, v70, 4
	v_pk_fma_f16 v79, v84, s60, v81 op_sel_hi:[1,0,1]
	v_pk_fma_f16 v81, v85, s60, v83 op_sel_hi:[1,0,1]
	v_pk_fma_f16 v7, v76, s60, v7 op_sel_hi:[1,0,1]
	v_and_b32_e32 v76, 0x7070707, v70
	v_and_b32_e32 v82, 0x7070707, v224
	v_perm_b32 v76, s2, v205, v76
	v_perm_b32 v82, s2, v205, v82
	v_and_or_b32 v76, v70, s4, v76
	v_and_or_b32 v70, v224, s4, v82
	v_perm_b32 v83, v70, v76, s33
	v_perm_b32 v84, v70, v76, s0
	v_perm_b32 v82, v70, v76, s5
	v_perm_b32 v70, v70, v76, s1
	v_pk_fma_f16 v76, v83, s36, v78 op_sel_hi:[1,0,1]
	v_pk_fma_f16 v78, v84, s36, v80 op_sel_hi:[1,0,1]
	s_add_u32 s66, s18, s64
	s_addc_u32 s67, s19, s65
	global_load_dwordx2 v[84:85], v121, s[66:67]
	v_alignbit_b32 v225, v71, v71, 4
	v_pk_fma_f16 v8, v70, s36, v8 op_sel_hi:[1,0,1]
	v_and_b32_e32 v70, 0x7070707, v71
	v_and_b32_e32 v80, 0x7070707, v225
	v_pk_fma_f16 v9, v82, s36, v9 op_sel_hi:[1,0,1]
	v_perm_b32 v70, s2, v205, v70
	v_perm_b32 v80, s2, v205, v80
	v_and_or_b32 v70, v71, s4, v70
	v_and_or_b32 v71, v225, s4, v80
	v_perm_b32 v80, v71, v70, s5
	v_perm_b32 v82, v71, v70, s33
	v_perm_b32 v83, v71, v70, s0
	v_perm_b32 v70, v71, v70, s1
	v_pk_fma_f16 v71, v80, s36, v77 op_sel_hi:[1,0,1]
	v_readlane_b32 s59, v120, 40
	s_waitcnt vmcnt(25)
	v_alignbit_b32 v224, v66, v66, 4
	v_pk_fma_f16 v77, v82, s36, v79 op_sel_hi:[1,0,1]
	v_pk_fma_f16 v79, v83, s36, v81 op_sel_hi:[1,0,1]
	v_pk_fma_f16 v7, v70, s36, v7 op_sel_hi:[1,0,1]
	v_and_b32_e32 v70, 0x7070707, v66
	v_and_b32_e32 v80, 0x7070707, v224
	v_perm_b32 v70, s2, v205, v70
	v_perm_b32 v80, s2, v205, v80
	v_and_or_b32 v70, v66, s4, v70
	v_and_or_b32 v66, v224, s4, v80
	v_perm_b32 v81, v66, v70, s33
	v_perm_b32 v82, v66, v70, s0
	v_perm_b32 v80, v66, v70, s5
	v_perm_b32 v66, v66, v70, s1
	v_pk_fma_f16 v70, v81, s59, v76 op_sel_hi:[1,0,1]
	v_pk_fma_f16 v76, v82, s59, v78 op_sel_hi:[1,0,1]
	s_add_u32 s66, s20, s64
	s_addc_u32 s67, s21, s65
	global_load_dwordx2 v[82:83], v121, s[66:67]
	v_alignbit_b32 v225, v67, v67, 4
	v_pk_fma_f16 v8, v66, s59, v8 op_sel_hi:[1,0,1]
	v_and_b32_e32 v66, 0x7070707, v67
	v_and_b32_e32 v78, 0x7070707, v225
	v_pk_fma_f16 v9, v80, s59, v9 op_sel_hi:[1,0,1]
	v_perm_b32 v66, s2, v205, v66
	v_perm_b32 v78, s2, v205, v78
	v_and_or_b32 v66, v67, s4, v66
	v_and_or_b32 v67, v225, s4, v78
	v_perm_b32 v78, v67, v66, s5
	v_perm_b32 v80, v67, v66, s33
	v_perm_b32 v81, v67, v66, s0
	v_perm_b32 v66, v67, v66, s1
	v_pk_fma_f16 v67, v78, s59, v71 op_sel_hi:[1,0,1]
	v_readlane_b32 s60, v120, 44
	s_waitcnt vmcnt(31)
	v_alignbit_b32 v224, v72, v72, 4
	v_pk_fma_f16 v71, v80, s59, v77 op_sel_hi:[1,0,1]
	v_pk_fma_f16 v77, v81, s59, v79 op_sel_hi:[1,0,1]
	v_pk_fma_f16 v7, v66, s59, v7 op_sel_hi:[1,0,1]
	v_and_b32_e32 v66, 0x7070707, v72
	v_and_b32_e32 v78, 0x7070707, v224
	v_perm_b32 v66, s2, v205, v66
	v_perm_b32 v78, s2, v205, v78
	v_and_or_b32 v66, v72, s4, v66
	v_and_or_b32 v72, v224, s4, v78
	v_perm_b32 v80, v72, v66, s0
	v_perm_b32 v78, v72, v66, s5
	v_perm_b32 v79, v72, v66, s33
	v_perm_b32 v66, v72, v66, s1
	v_pk_fma_f16 v72, v80, s60, v76 op_sel_hi:[1,0,1]
	s_add_u32 s66, s22, s64
	s_addc_u32 s67, s23, s65
	global_load_dwordx2 v[80:81], v121, s[66:67]
	v_alignbit_b32 v225, v73, v73, 4
	v_pk_fma_f16 v8, v66, s60, v8 op_sel_hi:[1,0,1]
	v_and_b32_e32 v66, 0x7070707, v73
	v_and_b32_e32 v76, 0x7070707, v225
	v_pk_fma_f16 v9, v78, s60, v9 op_sel_hi:[1,0,1]
	v_perm_b32 v66, s2, v205, v66
	v_perm_b32 v76, s2, v205, v76
	v_and_or_b32 v66, v73, s4, v66
	v_and_or_b32 v73, v225, s4, v76
	v_perm_b32 v76, v73, v66, s5
	v_pk_fma_f16 v70, v79, s60, v70 op_sel_hi:[1,0,1]
	v_perm_b32 v78, v73, v66, s33
	v_perm_b32 v79, v73, v66, s0
	v_perm_b32 v66, v73, v66, s1
	v_pk_fma_f16 v67, v76, s60, v67 op_sel_hi:[1,0,1]
	v_readlane_b32 s36, v120, 48
	s_waitcnt vmcnt(30)
	v_alignbit_b32 v224, v68, v68, 4
	v_pk_fma_f16 v71, v78, s60, v71 op_sel_hi:[1,0,1]
	v_pk_fma_f16 v73, v79, s60, v77 op_sel_hi:[1,0,1]
	v_pk_fma_f16 v7, v66, s60, v7 op_sel_hi:[1,0,1]
	v_and_b32_e32 v66, 0x7070707, v68
	v_and_b32_e32 v76, 0x7070707, v224
	v_perm_b32 v66, s2, v205, v66
	v_perm_b32 v76, s2, v205, v76
	v_and_or_b32 v66, v68, s4, v66
	v_and_or_b32 v68, v224, s4, v76
	v_perm_b32 v77, v68, v66, s33
	v_perm_b32 v78, v68, v66, s0
	v_perm_b32 v76, v68, v66, s5
	v_perm_b32 v66, v68, v66, s1
	v_pk_fma_f16 v68, v77, s36, v70 op_sel_hi:[1,0,1]
	v_pk_fma_f16 v70, v78, s36, v72 op_sel_hi:[1,0,1]
	s_add_u32 s66, s24, s64
	s_addc_u32 s67, s25, s65
	global_load_dwordx2 v[78:79], v121, s[66:67]
	v_alignbit_b32 v225, v69, v69, 4
	v_pk_fma_f16 v8, v66, s36, v8 op_sel_hi:[1,0,1]
	v_and_b32_e32 v66, 0x7070707, v69
	v_and_b32_e32 v72, 0x7070707, v225
	v_pk_fma_f16 v9, v76, s36, v9 op_sel_hi:[1,0,1]
	v_perm_b32 v66, s2, v205, v66
	v_perm_b32 v72, s2, v205, v72
	v_and_or_b32 v66, v69, s4, v66
	v_and_or_b32 v69, v225, s4, v72
	v_perm_b32 v72, v69, v66, s5
	v_perm_b32 v76, v69, v66, s33
	v_perm_b32 v77, v69, v66, s0
	v_perm_b32 v66, v69, v66, s1
	v_pk_fma_f16 v67, v72, s36, v67 op_sel_hi:[1,0,1]
	v_readlane_b32 s59, v120, 52
	s_waitcnt vmcnt(29)
	v_alignbit_b32 v224, v64, v64, 4
	v_pk_fma_f16 v69, v76, s36, v71 op_sel_hi:[1,0,1]
	v_pk_fma_f16 v71, v77, s36, v73 op_sel_hi:[1,0,1]
	v_pk_fma_f16 v7, v66, s36, v7 op_sel_hi:[1,0,1]
	v_and_b32_e32 v66, 0x7070707, v64
	v_and_b32_e32 v72, 0x7070707, v224
	v_perm_b32 v66, s2, v205, v66
	v_perm_b32 v72, s2, v205, v72
	v_and_or_b32 v66, v64, s4, v66
	v_and_or_b32 v64, v224, s4, v72
	v_perm_b32 v73, v64, v66, s33
	v_perm_b32 v76, v64, v66, s0
	v_perm_b32 v72, v64, v66, s5
	v_perm_b32 v64, v64, v66, s1
	v_pk_fma_f16 v66, v73, s59, v68 op_sel_hi:[1,0,1]
	v_pk_fma_f16 v68, v76, s59, v70 op_sel_hi:[1,0,1]
	s_add_u32 s66, s26, s64
	s_addc_u32 s67, s27, s65
	global_load_dwordx2 v[76:77], v121, s[66:67]
	v_alignbit_b32 v225, v65, v65, 4
	v_pk_fma_f16 v8, v64, s59, v8 op_sel_hi:[1,0,1]
	v_and_b32_e32 v64, 0x7070707, v65
	v_and_b32_e32 v70, 0x7070707, v225
	v_pk_fma_f16 v9, v72, s59, v9 op_sel_hi:[1,0,1]
	v_perm_b32 v64, s2, v205, v64
	v_perm_b32 v70, s2, v205, v70
	v_and_or_b32 v64, v65, s4, v64
	v_and_or_b32 v65, v225, s4, v70
	v_perm_b32 v70, v65, v64, s5
	v_perm_b32 v72, v65, v64, s33
	v_perm_b32 v73, v65, v64, s0
	v_perm_b32 v64, v65, v64, s1
	v_pk_fma_f16 v65, v70, s59, v67 op_sel_hi:[1,0,1]
	v_readlane_b32 s60, v120, 56
	s_waitcnt vmcnt(31)
	v_alignbit_b32 v224, v62, v62, 4
	v_pk_fma_f16 v67, v72, s59, v69 op_sel_hi:[1,0,1]
	v_pk_fma_f16 v69, v73, s59, v71 op_sel_hi:[1,0,1]
	v_pk_fma_f16 v7, v64, s59, v7 op_sel_hi:[1,0,1]
	v_and_b32_e32 v64, 0x7070707, v62
	v_and_b32_e32 v70, 0x7070707, v224
	v_perm_b32 v64, s2, v205, v64
	v_perm_b32 v70, s2, v205, v70
	v_and_or_b32 v64, v62, s4, v64
	v_and_or_b32 v62, v224, s4, v70
	v_perm_b32 v71, v62, v64, s33
	v_perm_b32 v72, v62, v64, s0
	v_perm_b32 v70, v62, v64, s5
	v_perm_b32 v62, v62, v64, s1
	v_pk_fma_f16 v64, v71, s60, v66 op_sel_hi:[1,0,1]
	v_pk_fma_f16 v66, v72, s60, v68 op_sel_hi:[1,0,1]
	s_add_u32 s66, s34, s64
	s_addc_u32 s67, s35, s65
	global_load_dwordx2 v[72:73], v121, s[66:67]
	v_alignbit_b32 v225, v63, v63, 4
	v_pk_fma_f16 v8, v62, s60, v8 op_sel_hi:[1,0,1]
	v_and_b32_e32 v62, 0x7070707, v63
	v_and_b32_e32 v68, 0x7070707, v225
	v_pk_fma_f16 v9, v70, s60, v9 op_sel_hi:[1,0,1]
	v_perm_b32 v62, s2, v205, v62
	v_perm_b32 v68, s2, v205, v68
	v_and_or_b32 v62, v63, s4, v62
	v_and_or_b32 v63, v225, s4, v68
	v_perm_b32 v68, v63, v62, s5
	v_perm_b32 v70, v63, v62, s33
	v_perm_b32 v71, v63, v62, s0
	v_perm_b32 v62, v63, v62, s1
	v_pk_fma_f16 v7, v62, s60, v7 op_sel_hi:[1,0,1]
	v_readlane_b32 s36, v120, 60
	s_waitcnt vmcnt(29)
	v_alignbit_b32 v224, v50, v50, 4
	v_pk_fma_f16 v63, v68, s60, v65 op_sel_hi:[1,0,1]
	v_pk_fma_f16 v65, v70, s60, v67 op_sel_hi:[1,0,1]
	v_pk_fma_f16 v67, v71, s60, v69 op_sel_hi:[1,0,1]
	s_add_u32 s66, s28, s64
	s_addc_u32 s67, s29, s65
	global_load_dwordx2 v[70:71], v121, s[66:67]
	v_and_b32_e32 v15, 0x7070707, v50
	v_and_b32_e32 v62, 0x7070707, v224
	v_perm_b32 v15, s2, v205, v15
	v_perm_b32 v62, s2, v205, v62
	v_and_or_b32 v15, v50, s4, v15
	v_and_or_b32 v50, v224, s4, v62
	v_perm_b32 v62, v50, v15, s5
	v_perm_b32 v68, v50, v15, s33
	v_perm_b32 v69, v50, v15, s0
	v_perm_b32 v15, v50, v15, s1
	v_pk_fma_f16 v105, v62, s36, v9 op_sel_hi:[1,0,1]
	v_alignbit_b32 v225, v51, v51, 4
	v_pk_fma_f16 v102, v15, s36, v8 op_sel_hi:[1,0,1]
	v_and_b32_e32 v8, 0x7070707, v51
	v_and_b32_e32 v9, 0x7070707, v225
	v_perm_b32 v8, s2, v205, v8
	v_perm_b32 v9, s2, v205, v9
	v_and_or_b32 v8, v51, s4, v8
	v_and_or_b32 v9, v225, s4, v9
	v_perm_b32 v15, v9, v8, s5
	v_perm_b32 v50, v9, v8, s33
	v_perm_b32 v51, v9, v8, s0
	v_perm_b32 v8, v9, v8, s1
	v_pk_fma_f16 v104, v68, s36, v64 op_sel_hi:[1,0,1]
	v_pk_fma_f16 v103, v69, s36, v66 op_sel_hi:[1,0,1]
	s_add_u32 s66, s38, s64
	s_addc_u32 s67, s39, s65
	global_load_dwordx2 v[68:69], v121, s[66:67]
	v_pk_fma_f16 v101, v15, s36, v63 op_sel_hi:[1,0,1]
	s_add_u32 s66, s52, s64
	s_addc_u32 s67, s53, s65
	global_load_dwordx2 v[62:63], v121, s[66:67]
	v_pk_fma_f16 v100, v50, s36, v65 op_sel_hi:[1,0,1]
	s_add_u32 s66, s50, s64
	s_addc_u32 s67, s51, s65
	global_load_dwordx2 v[64:65], v121, s[66:67]
	v_pk_fma_f16 v99, v51, s36, v67 op_sel_hi:[1,0,1]
	s_add_u32 s66, s30, s64
	s_addc_u32 s67, s31, s65
	global_load_dwordx2 v[66:67], v121, s[66:67]
	s_add_u32 s66, s54, s64
	s_addc_u32 s67, s55, s65
	global_load_dwordx2 v[50:51], v121, s[66:67]
	v_pk_fma_f16 v15, v8, s36, v7 op_sel_hi:[1,0,1]
	s_cmpk_eq_i32 s56, 0x90
	s_cbranch_scc0 .LBB0_770
	v_lshl_add_u64 v[94:95], v[2:3], 2, v[44:45]
	v_mov_b32_e32 v106, v208
	v_mov_b32_e32 v107, v209
	v_mov_b32_e32 v108, v210
	v_mov_b32_e32 v109, v211
	v_mov_b32_e32 v8, v212
	v_mov_b32_e32 v9, v213
	v_mov_b32_e32 v10, v214
	v_mov_b32_e32 v11, v215
	v_mov_b32_e32 v4, v216
	v_mov_b32_e32 v5, v217
	v_mov_b32_e32 v6, v218
	v_mov_b32_e32 v7, v219
	v_mov_b32_e32 v0, v220
	v_mov_b32_e32 v1, v221
	v_mov_b32_e32 v2, v222
	v_mov_b32_e32 v3, v223
	v_cvt_f32_f16_sdwa v13, v105 dst_sel:DWORD dst_unused:UNUSED_PAD src0_sel:WORD_1
	v_cvt_f32_f16_e32 v12, v105
	s_mov_b32 s12, 0x800000
	v_readlane_b32 s10, v255, 5
	v_readlane_b32 s11, v255, 6
	v_pk_add_f32 v[0:1], v[0:1], v[12:13]
	v_cvt_f32_f16_sdwa v13, v104 dst_sel:DWORD dst_unused:UNUSED_PAD src0_sel:WORD_1
	v_cvt_f32_f16_e32 v12, v104
	v_lshl_add_u64 v[48:49], v[48:49], 0, s[10:11]
	v_pk_add_f32 v[2:3], v[2:3], v[12:13]
	v_cvt_f32_f16_sdwa v13, v103 dst_sel:DWORD dst_unused:UNUSED_PAD src0_sel:WORD_1
	v_cvt_f32_f16_e32 v12, v103
	global_store_dwordx4 v[94:95], v[0:3], off
	v_pk_add_f32 v[4:5], v[4:5], v[12:13]
	v_cvt_f32_f16_sdwa v13, v102 dst_sel:DWORD dst_unused:UNUSED_PAD src0_sel:WORD_1
	v_cvt_f32_f16_e32 v12, v102
	v_mov_b32_e32 v102, v1
	v_mov_b32_e32 v103, v5
	v_pk_mul_f32 v[102:103], v[102:103], v[102:103]
	v_pk_add_f32 v[6:7], v[6:7], v[12:13]
	v_mov_b32_e32 v12, v0
	v_mov_b32_e32 v13, v4
	v_pk_fma_f32 v[12:13], v[12:13], v[12:13], v[102:103]
	v_mov_b32_e32 v102, v2
	v_mov_b32_e32 v103, v6
	v_pk_fma_f32 v[12:13], v[102:103], v[102:103], v[12:13]
	v_mov_b32_e32 v102, v3
	v_mov_b32_e32 v103, v7
	v_pk_fma_f32 v[102:103], v[102:103], v[102:103], v[12:13]
	v_cvt_f32_f16_sdwa v13, v101 dst_sel:DWORD dst_unused:UNUSED_PAD src0_sel:WORD_1
	v_cvt_f32_f16_e32 v12, v101
	v_cvt_f32_f16_sdwa v101, v15 dst_sel:DWORD dst_unused:UNUSED_PAD src0_sel:WORD_1
	global_store_dwordx4 v[94:95], v[4:7], off offset:16
	v_pk_add_f32 v[8:9], v[8:9], v[12:13]
	v_cvt_f32_f16_sdwa v13, v100 dst_sel:DWORD dst_unused:UNUSED_PAD src0_sel:WORD_1
	v_cvt_f32_f16_e32 v12, v100
	v_cvt_f32_f16_e32 v100, v15
	v_pk_add_f32 v[10:11], v[10:11], v[12:13]
	v_cvt_f32_f16_sdwa v13, v99 dst_sel:DWORD dst_unused:UNUSED_PAD src0_sel:WORD_1
	v_cvt_f32_f16_e32 v12, v99
	v_pk_add_f32 v[14:15], v[108:109], v[100:101]
	v_mov_b32_e32 v100, v9
	global_store_dwordx4 v[94:95], v[8:11], off offset:32
	v_pk_add_f32 v[12:13], v[106:107], v[12:13]
	global_store_dwordx4 v[94:95], v[12:15], off offset:48
	v_mov_b32_e32 v101, v13
	v_mov_b32_e32 v94, v8
	v_mov_b32_e32 v95, v12
	v_pk_mul_f32 v[100:101], v[100:101], v[100:101]
	v_add_f32_e32 v99, v102, v103
	v_pk_fma_f32 v[94:95], v[94:95], v[94:95], v[100:101]
	v_mov_b32_e32 v100, v10
	v_mov_b32_e32 v101, v14
	v_pk_fma_f32 v[94:95], v[100:101], v[100:101], v[94:95]
	v_mov_b32_e32 v100, v11
	v_mov_b32_e32 v101, v15
	v_pk_fma_f32 v[94:95], v[100:101], v[100:101], v[94:95]
	global_load_dwordx4 v[100:103], v[46:47], off offset:48
	global_load_dwordx4 v[104:107], v[46:47], off offset:32
	global_load_dwordx4 v[108:111], v[46:47], off offset:16
	global_load_dwordx4 v[112:115], v[46:47], off
	v_add_f32_e32 v94, v99, v94
	v_add_f32_e32 v94, v94, v95
	v_mov_b32_e32 v95, v94
	s_nop 1
	v_permlane32_swap_b32 v95, v94
	s_waitcnt lgkmcnt(0)
	v_add_f32_e32 v94, v94, v95
	v_mov_b32_e32 v95, v94
	s_nop 1
	v_permlane16_swap_b32 v95, v94
	s_waitcnt lgkmcnt(0)
	v_add_f32_e32 v94, v94, v95
	s_nop 1
	v_mov_b32_dpp v95, v94 row_ror:8 row_mask:0xf bank_mask:0xf
	s_waitcnt lgkmcnt(0)
	v_add_f32_e32 v94, v94, v95
	s_nop 1
	v_mov_b32_dpp v95, v94 row_half_mirror row_mask:0xf bank_mask:0xf
	s_nop 1
	v_mov_b32_dpp v95, v95 quad_perm:[3,2,1,0] row_mask:0xf bank_mask:0xf
	s_waitcnt lgkmcnt(0)
	v_add_f32_e32 v94, v94, v95
	s_nop 1
	v_mov_b32_dpp v95, v94 quad_perm:[2,3,0,1] row_mask:0xf bank_mask:0xf
	s_waitcnt lgkmcnt(0)
	v_add_f32_e32 v94, v94, v95
	s_nop 1
	v_mov_b32_dpp v95, v94 quad_perm:[1,0,3,2] row_mask:0xf bank_mask:0xf
	s_waitcnt lgkmcnt(0)
	v_add_f32_e32 v94, v94, v95
	v_fmamk_f32 v94, v94, 0x3a800000, v191
	v_cmp_gt_f32_e32 vcc, s12, v94
	v_mul_f32_e32 v95, 0x4b800000, v94
	s_nop 0
	v_cndmask_b32_e32 v94, v94, v95, vcc
	v_rsq_f32_e32 v94, v94
	s_nop 0
	v_mul_f32_e32 v95, 0x45800000, v94
	v_cndmask_b32_e32 v94, v94, v95, vcc
	v_pk_mul_f32 v[0:1], v[0:1], v[94:95] op_sel_hi:[1,0]
	v_pk_mul_f32 v[2:3], v[2:3], v[94:95] op_sel_hi:[1,0]
	s_waitcnt vmcnt(0)
	v_pk_mul_f32 v[0:1], v[112:113], v[0:1]
	v_pk_mul_f32 v[2:3], v[114:115], v[2:3]
	v_cvt_pk_bf16_f32 v0, v0, v1
	v_cvt_pk_bf16_f32 v1, v2, v3
	v_pk_mul_f32 v[2:3], v[4:5], v[94:95] op_sel_hi:[1,0]
	v_pk_mul_f32 v[4:5], v[6:7], v[94:95] op_sel_hi:[1,0]
	v_pk_mul_f32 v[2:3], v[108:109], v[2:3]
	v_pk_mul_f32 v[4:5], v[110:111], v[4:5]
	v_cvt_pk_bf16_f32 v2, v2, v3
	v_cvt_pk_bf16_f32 v3, v4, v5
	v_pk_mul_f32 v[4:5], v[8:9], v[94:95] op_sel_hi:[1,0]
	v_pk_mul_f32 v[6:7], v[10:11], v[94:95] op_sel_hi:[1,0]
	v_pk_mul_f32 v[4:5], v[104:105], v[4:5]
	v_pk_mul_f32 v[6:7], v[6:7], v[106:107]
	v_cvt_pk_bf16_f32 v4, v4, v5
	v_cvt_pk_bf16_f32 v5, v6, v7
	v_pk_mul_f32 v[6:7], v[12:13], v[94:95] op_sel_hi:[1,0]
	v_pk_mul_f32 v[8:9], v[14:15], v[94:95] op_sel_hi:[1,0]
	v_pk_mul_f32 v[6:7], v[6:7], v[100:101]
	v_pk_mul_f32 v[8:9], v[8:9], v[102:103]
	v_cvt_pk_bf16_f32 v6, v6, v7
	v_cvt_pk_bf16_f32 v7, v8, v9
	global_store_dwordx4 v[74:75], v[0:3], off
	global_store_dwordx4 v[74:75], v[4:7], off offset:16
	s_nop 0
	v_mov_b32_e32 v0, v98
	s_andn2_b64 exec, exec, s[8:9]
	s_cbranch_execnz .LBB0_769
